# speedup vs baseline: 1.0112x; 1.0029x over previous
.LBB7_3:
	s_ashr_i32 s44, s23, 31
	s_xor_b32 s44, s44, s25
	s_abs_i32 s45, s23
	s_mul_hi_u32 s48, s45, s26
	s_mul_i32 s49, s48, s24
	s_sub_i32 s45, s45, s49
	s_add_i32 s49, s48, 1
	s_sub_i32 s46, s45, s24
	s_cmp_ge_u32 s45, s24
	s_cselect_b32 s48, s49, s48
	s_cselect_b32 s45, s46, s45
	s_add_i32 s49, s48, 1
	s_cmp_ge_u32 s45, s24
	s_cselect_b32 s45, s49, s48
	s_xor_b32 s45, s45, s44
	s_sub_i32 s44, s45, s44
	s_mul_i32 s45, s44, s21
	s_sub_i32 s47, s23, s45
	s_lshl_b32 s48, s47, 7
	s_lshl_b32 s46, s44, 7
	s_ashr_i32 s49, s48, 31
	v_or_b32_e32 v152, s46, v1
	v_lshl_add_u64 v[154:155], s[48:49], 1, v[70:71]
	v_mad_i64_i32 v[156:157], s[50:51], v152, s29, v[154:155]
	v_lshl_add_u64 v[158:159], s[48:49], 2, v[68:69]
	v_or_b32_e32 v153, 32, v152
	global_load_dwordx4 v[160:163], v[156:157], off
	v_mad_i64_i32 v[184:185], s[50:51], v153, s29, v[154:155]
	v_or_b32_e32 v153, 64, v152
	global_load_dwordx4 v[176:179], v[158:159], off
	global_load_dwordx4 v[180:183], v[158:159], off offset:16
	v_mad_i64_i32 v[186:187], s[50:51], v153, s29, v[154:155]
	v_or_b32_e32 v153, 0x60, v152
	global_load_dwordx4 v[164:167], v[184:185], off
	v_mad_i64_i32 v[188:189], s[50:51], v153, s29, v[154:155]
	global_load_dwordx4 v[168:171], v[186:187], off
	s_nop 0
	global_load_dwordx4 v[172:175], v[188:189], off
	v_add_u32_e32 v67, v80, v77
	s_waitcnt vmcnt(14)
	s_barrier
	s_waitcnt lgkmcnt(0)
	ds_read_b128 v[2:5], v67 offset:16384
	v_add_u32_e32 v109, v79, v77
	ds_read_b128 v[6:9], v109
	ds_read_b128 v[10:13], v109 offset:4096
	ds_read_b128 v[14:17], v67 offset:20480
	v_add_u32_e32 v126, v80, v76
	ds_read_b128 v[34:37], v126 offset:16384
	v_add_u32_e32 v127, v79, v76
	s_waitcnt lgkmcnt(3)
	v_mfma_f32_32x32x16_f16 v[50:65], v[2:5], v[6:9], 0
	ds_read_b128 v[110:113], v127
	ds_read_b128 v[114:117], v127 offset:4096
	ds_read_b128 v[118:121], v126 offset:20480
	v_readfirstlane_b32 s2, v0
	s_lshl_b32 s19, s27, 15
	s_lshl_b32 s2, s2, 4
	s_add_i32 s1, s19, 0
	s_and_b32 s31, s2, 0xfffffc00
	s_add_i32 s1, s1, s31
	s_waitcnt lgkmcnt(5)
	v_mfma_f32_32x32x16_f16 v[18:33], v[2:5], v[10:13], 0
	s_mov_b32 m0, s1
	s_add_i32 s2, s1, 0x2000
	buffer_load_dwordx4 v72, s[4:7], s0 offen lds
	s_mov_b32 m0, s2
	s_add_i32 s3, s1, 0x4000
	buffer_load_dwordx4 v74, s[4:7], s0 offen lds
	s_mov_b32 s14, s10
	s_waitcnt lgkmcnt(2)
	v_mfma_f32_32x32x16_f16 v[50:65], v[34:37], v[110:113], v[50:65]
	s_mov_b32 s15, s11
	s_mov_b32 m0, s3
	s_add_i32 s18, s1, 0x6000
	buffer_load_dwordx4 v73, s[12:15], s0 offen lds
	s_mov_b32 m0, s18
	s_add_i32 s33, s19, 0x8000
	buffer_load_dwordx4 v75, s[12:15], s0 offen lds
	s_waitcnt lgkmcnt(1)
	v_mfma_f32_32x32x16_f16 v[18:33], v[34:37], v[114:117], v[18:33]
	s_waitcnt vmcnt(14)
	s_barrier
	s_and_b32 s33, s33, 0x18000
	s_add_i32 s33, s33, 0
	s_add_i32 s33, s33, s31
	s_add_i32 s34, s0, 0x80
	s_mov_b32 m0, s33
	v_mfma_f32_32x32x16_f16 v[34:49], v[14:17], v[6:9], 0
	v_add_u32_e32 v128, v81, v77
	v_add_u32_e32 v129, v82, v77
	v_add_u32_e32 v130, v81, v76
	v_add_u32_e32 v131, v82, v76
	s_xor_b32 s19, s19, 0x10000
	v_add_u32_e32 v134, v83, v77
	v_add_u32_e32 v138, v84, v77
	v_mfma_f32_32x32x16_f16 v[2:17], v[14:17], v[10:13], 0
	v_add_u32_e32 v142, v83, v76
	v_add_u32_e32 v146, v84, v76
	s_waitcnt lgkmcnt(0)
	v_mfma_f32_32x32x16_f16 v[34:49], v[118:121], v[110:113], v[34:49]
	v_mfma_f32_32x32x16_f16 v[2:17], v[118:121], v[114:117], v[2:17]
	ds_read_b128 v[110:113], v67 offset:49152
	ds_read_b128 v[114:117], v109 offset:32768
	ds_read_b128 v[118:121], v109 offset:36864
	ds_read_b128 v[122:125], v67 offset:53248
	s_waitcnt lgkmcnt(2)
	v_mfma_f32_32x32x16_f16 v[50:65], v[110:113], v[114:117], v[50:65]
	s_waitcnt lgkmcnt(1)
	v_mfma_f32_32x32x16_f16 v[18:33], v[110:113], v[118:121], v[18:33]
	s_waitcnt lgkmcnt(0)
	v_mfma_f32_32x32x16_f16 v[34:49], v[122:125], v[114:117], v[34:49]
	v_mfma_f32_32x32x16_f16 v[2:17], v[122:125], v[118:121], v[2:17]
	ds_read_b128 v[110:113], v126 offset:49152
	ds_read_b128 v[114:117], v127 offset:32768
	ds_read_b128 v[118:121], v127 offset:36864
	ds_read_b128 v[122:125], v126 offset:53248
	buffer_load_dwordx4 v72, s[4:7], s34 offen lds
	s_add_i32 m0, s33, 0x2000
	s_nop 0
	buffer_load_dwordx4 v74, s[4:7], s34 offen lds
	s_add_i32 m0, s33, 0x4000
	s_nop 0
	buffer_load_dwordx4 v73, s[12:15], s34 offen lds
	s_add_i32 m0, s33, 0x6000
	s_waitcnt lgkmcnt(2)
	v_mfma_f32_32x32x16_f16 v[50:65], v[110:113], v[114:117], v[50:65]
	buffer_load_dwordx4 v75, s[12:15], s34 offen lds
	s_waitcnt vmcnt(14)
	s_barrier
	s_add_i32 s33, s19, 0
	s_add_i32 s33, s33, s31
	s_add_i32 s34, s0, 0x100
	s_mov_b32 m0, s33
	s_waitcnt lgkmcnt(1)
	v_mfma_f32_32x32x16_f16 v[18:33], v[110:113], v[118:121], v[18:33]
	ds_read_b128 v[110:113], v96
	s_add_i32 s19, s19, 0x8000
	s_and_b32 s19, s19, 0x18000
	s_add_i32 s19, s19, 0
	s_add_i32 s19, s19, s31
	s_add_i32 s31, s0, 0x180
	s_waitcnt lgkmcnt(1)
	v_mfma_f32_32x32x16_f16 v[34:49], v[122:125], v[114:117], v[34:49]
	v_mfma_f32_32x32x16_f16 v[2:17], v[122:125], v[118:121], v[2:17]
	ds_read_b128 v[114:117], v128
	ds_read_b128 v[118:121], v128 offset:4096
	ds_read_b128 v[122:125], v129 offset:4096
	s_waitcnt lgkmcnt(2)
	v_mfma_f32_32x32x16_f16 v[50:65], v[110:113], v[114:117], v[50:65]
	s_waitcnt lgkmcnt(1)
	v_mfma_f32_32x32x16_f16 v[18:33], v[110:113], v[118:121], v[18:33]
	ds_read_b128 v[110:113], v97
	s_waitcnt lgkmcnt(1)
	v_mfma_f32_32x32x16_f16 v[34:49], v[122:125], v[114:117], v[34:49]
	v_mfma_f32_32x32x16_f16 v[2:17], v[122:125], v[118:121], v[2:17]
	ds_read_b128 v[114:117], v130
	ds_read_b128 v[118:121], v130 offset:4096
	ds_read_b128 v[122:125], v131 offset:4096
	buffer_load_dwordx4 v72, s[4:7], s34 offen lds
	s_add_i32 m0, s33, 0x2000
	s_nop 0
	buffer_load_dwordx4 v74, s[4:7], s34 offen lds
	s_add_i32 m0, s33, 0x4000
	s_waitcnt lgkmcnt(2)
	v_mfma_f32_32x32x16_f16 v[50:65], v[110:113], v[114:117], v[50:65]
	buffer_load_dwordx4 v73, s[12:15], s34 offen lds
	s_add_i32 m0, s33, 0x6000
	s_nop 0
	buffer_load_dwordx4 v75, s[12:15], s34 offen lds
	s_waitcnt vmcnt(8)
	s_barrier
	s_mov_b32 m0, s19
	s_waitcnt lgkmcnt(1)
	v_mfma_f32_32x32x16_f16 v[18:33], v[110:113], v[118:121], v[18:33]
	ds_read_b128 v[110:113], v98
	s_waitcnt lgkmcnt(1)
	v_mfma_f32_32x32x16_f16 v[34:49], v[122:125], v[114:117], v[34:49]
	v_mfma_f32_32x32x16_f16 v[2:17], v[122:125], v[118:121], v[2:17]
	ds_read_b128 v[114:117], v134
	ds_read_b128 v[118:121], v134 offset:4096
	ds_read_b128 v[122:125], v138 offset:4096
	s_waitcnt lgkmcnt(2)
	v_mfma_f32_32x32x16_f16 v[50:65], v[110:113], v[114:117], v[50:65]
	s_waitcnt lgkmcnt(1)
	v_mfma_f32_32x32x16_f16 v[18:33], v[110:113], v[118:121], v[18:33]
	ds_read_b128 v[110:113], v99
	s_waitcnt lgkmcnt(1)
	v_mfma_f32_32x32x16_f16 v[34:49], v[122:125], v[114:117], v[34:49]
	v_mfma_f32_32x32x16_f16 v[2:17], v[122:125], v[118:121], v[2:17]
	ds_read_b128 v[114:117], v142
	ds_read_b128 v[118:121], v142 offset:4096
	ds_read_b128 v[122:125], v146 offset:4096
	buffer_load_dwordx4 v72, s[4:7], s31 offen lds
	s_add_i32 m0, s19, 0x2000
	s_nop 0
	buffer_load_dwordx4 v74, s[4:7], s31 offen lds
	s_add_i32 m0, s19, 0x4000
	s_waitcnt lgkmcnt(2)
	v_mfma_f32_32x32x16_f16 v[50:65], v[110:113], v[114:117], v[50:65]
	buffer_load_dwordx4 v73, s[12:15], s31 offen lds
	s_add_i32 m0, s19, 0x6000
	s_nop 0
	buffer_load_dwordx4 v75, s[12:15], s31 offen lds
	s_waitcnt vmcnt(8)
	s_barrier
	s_add_i32 s31, s0, 0x200
	s_waitcnt lgkmcnt(1)
	v_mfma_f32_32x32x16_f16 v[18:33], v[110:113], v[118:121], v[18:33]
	s_mov_b32 m0, s1
	s_abs_i32 s1, s23
	s_ashr_i32 s0, s23, 31
	s_xor_b32 s0, s0, s25
	s_waitcnt lgkmcnt(0)
	v_mfma_f32_32x32x16_f16 v[2:17], v[122:125], v[118:121], v[2:17]
	v_mfma_f32_32x32x16_f16 v[34:49], v[122:125], v[114:117], v[34:49]
	ds_read_b128 v[110:113], v67 offset:16384
	ds_read_b128 v[114:117], v109
	ds_read_b128 v[118:121], v109 offset:4096
	ds_read_b128 v[122:125], v67 offset:20480
	s_waitcnt lgkmcnt(2)
	v_mfma_f32_32x32x16_f16 v[50:65], v[110:113], v[114:117], v[50:65]
	s_waitcnt lgkmcnt(1)
	v_mfma_f32_32x32x16_f16 v[18:33], v[110:113], v[118:121], v[18:33]
	s_waitcnt lgkmcnt(0)
	v_mfma_f32_32x32x16_f16 v[2:17], v[122:125], v[118:121], v[2:17]
	v_mfma_f32_32x32x16_f16 v[34:49], v[122:125], v[114:117], v[34:49]
	ds_read_b128 v[110:113], v126 offset:16384
	ds_read_b128 v[114:117], v127
	ds_read_b128 v[118:121], v127 offset:4096
	ds_read_b128 v[122:125], v126 offset:20480
	buffer_load_dwordx4 v72, s[4:7], s31 offen lds
	s_mov_b32 m0, s2
	s_mul_hi_u32 s2, s1, s26
	buffer_load_dwordx4 v74, s[4:7], s31 offen lds
	s_mov_b32 m0, s3
	s_mul_i32 s3, s2, s24
	s_waitcnt lgkmcnt(2)
	v_mfma_f32_32x32x16_f16 v[50:65], v[110:113], v[114:117], v[50:65]
	buffer_load_dwordx4 v73, s[12:15], s31 offen lds
	s_mov_b32 m0, s18
	s_sub_i32 s1, s1, s3
	buffer_load_dwordx4 v75, s[12:15], s31 offen lds
	s_waitcnt vmcnt(8)
	s_barrier
	s_add_i32 s3, s2, 1
	s_waitcnt lgkmcnt(1)
	v_mfma_f32_32x32x16_f16 v[18:33], v[110:113], v[118:121], v[18:33]
	s_sub_i32 s14, s1, s24
	s_cmp_ge_u32 s1, s24
	s_cselect_b32 s2, s3, s2
	s_cselect_b32 s1, s14, s1
	s_add_i32 s3, s2, 1
	s_cmp_ge_u32 s1, s24
	s_cselect_b32 s1, s3, s2
	s_waitcnt lgkmcnt(0)
	v_mfma_f32_32x32x16_f16 v[2:17], v[122:125], v[118:121], v[2:17]
	s_xor_b32 s1, s1, s0
	s_sub_i32 s0, s1, s0
	s_mul_i32 s1, s0, s21
	s_sub_i32 s15, s23, s1
	s_lshl_b32 s2, s15, 7
	s_lshl_b32 s14, s0, 7
	s_ashr_i32 s3, s2, 31
	v_mfma_f32_32x32x16_f16 v[34:49], v[122:125], v[114:117], v[34:49]
	ds_read_b128 v[110:113], v67 offset:49152
	ds_read_b128 v[114:117], v109 offset:32768
	ds_read_b128 v[118:121], v109 offset:36864
	ds_read_b128 v[122:125], v67 offset:53248
	s_waitcnt lgkmcnt(2)
	v_mfma_f32_32x32x16_f16 v[50:65], v[110:113], v[114:117], v[50:65]
	s_waitcnt lgkmcnt(1)
	v_mfma_f32_32x32x16_f16 v[18:33], v[110:113], v[118:121], v[18:33]
	s_waitcnt lgkmcnt(0)
	v_mfma_f32_32x32x16_f16 v[2:17], v[122:125], v[118:121], v[2:17]
	v_mfma_f32_32x32x16_f16 v[34:49], v[122:125], v[114:117], v[34:49]
	ds_read_b128 v[110:113], v126 offset:49152
	ds_read_b128 v[114:117], v127 offset:32768
	ds_read_b128 v[118:121], v127 offset:36864
	ds_read_b128 v[122:125], v126 offset:53248
	s_waitcnt vmcnt(4)
	s_barrier
	s_waitcnt lgkmcnt(2)
	v_mfma_f32_32x32x16_f16 v[50:65], v[110:113], v[114:117], v[50:65]
	s_waitcnt lgkmcnt(1)
	v_mfma_f32_32x32x16_f16 v[18:33], v[110:113], v[118:121], v[18:33]
	s_waitcnt lgkmcnt(0)
	v_mfma_f32_32x32x16_f16 v[2:17], v[122:125], v[118:121], v[2:17]
	v_mfma_f32_32x32x16_f16 v[34:49], v[122:125], v[114:117], v[34:49]
	ds_read_b128 v[110:113], v96
	ds_read_b128 v[114:117], v128
	ds_read_b128 v[118:121], v128 offset:4096
	ds_read_b128 v[122:125], v129 offset:4096
	s_waitcnt lgkmcnt(2)
	v_mfma_f32_32x32x16_f16 v[50:65], v[110:113], v[114:117], v[50:65]
	s_waitcnt lgkmcnt(1)
	v_mfma_f32_32x32x16_f16 v[18:33], v[110:113], v[118:121], v[18:33]
	s_waitcnt lgkmcnt(0)
	v_mfma_f32_32x32x16_f16 v[2:17], v[122:125], v[118:121], v[2:17]
	v_mfma_f32_32x32x16_f16 v[34:49], v[122:125], v[114:117], v[34:49]
	ds_read_b128 v[110:113], v97
	ds_read_b128 v[114:117], v130
	ds_read_b128 v[126:129], v130 offset:4096
	ds_read_b128 v[130:133], v131 offset:4096
	s_waitcnt vmcnt(0)
	s_barrier
	s_waitcnt lgkmcnt(2)
	v_mfma_f32_32x32x16_f16 v[50:65], v[110:113], v[114:117], v[50:65]
	s_waitcnt lgkmcnt(1)
	v_mfma_f32_32x32x16_f16 v[18:33], v[110:113], v[126:129], v[18:33]
	s_waitcnt lgkmcnt(0)
	v_mfma_f32_32x32x16_f16 v[2:17], v[130:133], v[126:129], v[2:17]
	v_mfma_f32_32x32x16_f16 v[34:49], v[130:133], v[114:117], v[34:49]
	ds_read_b128 v[110:113], v98
	ds_read_b128 v[114:117], v134
	ds_read_b128 v[134:137], v134 offset:4096
	ds_read_b128 v[138:141], v138 offset:4096
	s_waitcnt lgkmcnt(2)
	v_mfma_f32_32x32x16_f16 v[50:65], v[110:113], v[114:117], v[50:65]
	s_waitcnt lgkmcnt(1)
	v_mfma_f32_32x32x16_f16 v[18:33], v[110:113], v[134:137], v[18:33]
	s_waitcnt lgkmcnt(0)
	v_mfma_f32_32x32x16_f16 v[2:17], v[138:141], v[134:137], v[2:17]
	v_mfma_f32_32x32x16_f16 v[34:49], v[138:141], v[114:117], v[34:49]
	ds_read_b128 v[110:113], v99
	ds_read_b128 v[114:117], v142
	ds_read_b128 v[142:145], v142 offset:4096
	ds_read_b128 v[146:149], v146 offset:4096
	s_waitcnt lgkmcnt(0)
	s_barrier
	s_waitcnt lgkmcnt(2)
	v_mfma_f32_32x32x16_f16 v[50:65], v[110:113], v[114:117], v[50:65]
	s_nop 11
	ds_write_b128 v100, v[50:53]
	ds_write_b128 v101, v[54:57]
	s_waitcnt lgkmcnt(3)
	v_mfma_f32_32x32x16_f16 v[18:33], v[110:113], v[142:145], v[18:33]
	s_waitcnt lgkmcnt(2)
	v_mfma_f32_32x32x16_f16 v[2:17], v[146:149], v[142:145], v[2:17]
	v_mfma_f32_32x32x16_f16 v[34:49], v[146:149], v[114:117], v[34:49]
	ds_write_b128 v102, v[58:61]
	ds_write_b128 v103, v[62:65]
	s_nop 9
	ds_write_b128 v104, v[34:37]
	ds_write_b128 v105, v[38:41]
	ds_write_b128 v106, v[42:45]
	ds_write_b128 v107, v[46:49]
	ds_write_b128 v100, v[18:21] offset:16384
	ds_write_b128 v101, v[22:25] offset:16384
	ds_write_b128 v102, v[26:29] offset:16384
	ds_write_b128 v103, v[30:33] offset:16384
	ds_write_b128 v104, v[2:5] offset:16384
	ds_write_b128 v105, v[6:9] offset:16384
	ds_write_b128 v106, v[10:13] offset:16384
	ds_write_b128 v107, v[14:17] offset:16384
	v_or_b32_e32 v25, s14, v1
	s_waitcnt lgkmcnt(0)
	s_barrier
	v_mov_b64_e32 v[10:11], v[160:161]
	v_mov_b64_e32 v[12:13], v[162:163]
	v_mov_b64_e32 v[6:7], v[176:177]
	v_mov_b64_e32 v[8:9], v[178:179]
	v_mov_b64_e32 v[2:3], v[180:181]
	v_mov_b64_e32 v[4:5], v[182:183]
	v_add_u32_e32 v14, 0, v85
	v_add_u32_e32 v18, s28, v85
	ds_read_b128 v[14:17], v14
	ds_read_b128 v[26:29], v18
	v_mov_b64_e32 v[18:19], v[164:165]
	v_mov_b64_e32 v[20:21], v[166:167]
	s_waitcnt lgkmcnt(0)
	v_pk_add_f32 v[16:17], v[16:17], v[28:29]
	v_add_f32_e32 v35, v14, v26
	v_mov_b32_e32 v34, v27
	v_cvt_f32_f16_e32 v30, v11
	v_cvt_f32_f16_sdwa v31, v11 dst_sel:DWORD dst_unused:UNUSED_PAD src0_sel:WORD_1
	v_add_u32_e32 v11, 0, v86
	v_pk_add_f32 v[16:17], v[8:9], v[16:17]
	ds_read_b128 v[26:29], v11
	v_add_u32_e32 v11, s28, v86
	v_pk_add_f32 v[36:37], v[16:17], v[30:31]
	ds_read_b128 v[30:33], v11
	v_cvt_f32_f16_e32 v38, v13
	v_cvt_f32_f16_sdwa v39, v13 dst_sel:DWORD dst_unused:UNUSED_PAD src0_sel:WORD_1
	v_mov_b32_e32 v16, v2
	v_mov_b32_e32 v17, v3
	s_waitcnt lgkmcnt(0)
	v_pk_add_f32 v[28:29], v[28:29], v[32:33]
	v_cvt_f32_f16_e32 v32, v10
	v_pk_add_f32 v[28:29], v[4:5], v[28:29]
	v_pk_mov_b32 v[16:17], v[26:27], v[16:17] op_sel:[1,0]
	v_pk_add_f32 v[28:29], v[28:29], v[38:39]
	v_cvt_f32_f16_e32 v38, v12
	v_add_f32_e32 v26, v26, v30
	v_cvt_f32_f16_sdwa v33, v10 dst_sel:DWORD dst_unused:UNUSED_PAD src0_sel:WORD_1
	v_cvt_f32_f16_sdwa v30, v12 dst_sel:DWORD dst_unused:UNUSED_PAD src0_sel:WORD_1
	v_pk_mov_b32 v[14:15], v[14:15], v[6:7] op_sel:[1,0]
	v_mov_b32_e32 v10, v31
	v_mov_b32_e32 v11, v26
	v_pk_add_f32 v[44:45], v[14:15], v[34:35]
	v_mov_b32_e32 v12, v7
	v_mov_b32_e32 v13, v32
	v_pk_add_f32 v[10:11], v[16:17], v[10:11]
	v_pk_add_f32 v[46:47], v[12:13], v[44:45]
	v_mov_b32_e32 v22, v3
	v_mov_b32_e32 v23, v38
	v_pk_add_f32 v[48:49], v[22:23], v[10:11]
	v_mov_b32_e32 v10, v33
	v_mov_b32_e32 v11, v47
	v_pk_add_f32 v[50:51], v[46:47], v[10:11]
	v_mov_b64_e32 v[14:15], v[168:169]
	v_mov_b64_e32 v[16:17], v[170:171]
	v_mov_b64_e32 v[10:11], v[172:173]
	v_mov_b64_e32 v[12:13], v[174:175]
	v_mov_b32_e32 v31, v49
	v_pk_add_f32 v[40:41], v[48:49], v[30:31]
	v_pk_mov_b32 v[30:31], v[34:35], v[44:45] op_sel:[1,0]
	v_mov_b32_e32 v27, v44
	v_mov_b32_e32 v3, v7
	v_pk_add_f32 v[30:31], v[6:7], v[30:31]
	v_mov_b32_e32 v39, v33
	v_pk_add_f32 v[26:27], v[2:3], v[26:27]
	v_pk_add_f32 v[30:31], v[30:31], v[32:33]
	v_pk_add_f32 v[26:27], v[26:27], v[38:39]
	v_pk_mul_f32 v[32:33], v[46:47], v[46:47]
	v_pk_add_f32 v[34:35], v[30:31], v[26:27]
	v_pk_mul_f32 v[26:27], v[30:31], v[26:27]
	v_mov_b32_e32 v51, v33
	v_pk_mul_f32 v[32:33], v[48:49], v[48:49]
	v_mov_b32_e32 v35, v27
	v_pk_mul_f32 v[26:27], v[40:41], v[40:41]
	v_mov_b32_e32 v32, v40
	v_mov_b32_e32 v67, v26
	v_pk_add_f32 v[32:33], v[50:51], v[32:33]
	v_pk_add_f32 v[26:27], v[34:35], v[66:67]
	v_pk_mul_f32 v[30:31], v[36:37], v[36:37]
	v_pk_mul_f32 v[34:35], v[28:29], v[28:29]
	v_pk_add_f32 v[26:27], v[32:33], v[26:27]
	v_mov_b32_e32 v32, v36
	v_mov_b32_e32 v33, v30
	v_mov_b32_e32 v38, v28
	v_mov_b32_e32 v39, v34
	v_pk_add_f32 v[32:33], v[32:33], v[38:39]
	v_mov_b32_e32 v30, v37
	v_mov_b32_e32 v34, v29
	v_pk_add_f32 v[26:27], v[26:27], v[32:33]
	v_pk_add_f32 v[30:31], v[30:31], v[34:35]
	v_pk_add_f32 v[26:27], v[26:27], v[30:31]
	s_nop 1
	v_mov_b32_dpp v32, v26 row_mirror row_mask:0xf bank_mask:0xf
	v_mov_b32_dpp v33, v27 row_mirror row_mask:0xf bank_mask:0xf
	v_cvt_pk_f16_f32 v39, v28, v29
	v_or_b32_e32 v31, s2, v78
	s_waitcnt lgkmcnt(0)
	v_pk_add_f32 v[26:27], v[26:27], v[32:33]
	s_nop 1
	v_mov_b32_dpp v34, v26 row_half_mirror row_mask:0xf bank_mask:0xf
	v_mov_b32_dpp v35, v27 row_half_mirror row_mask:0xf bank_mask:0xf
	v_cvt_pk_f16_f32 v37, v36, v37
	v_cvt_pk_f16_f32 v36, v47, v50
	s_waitcnt lgkmcnt(0)
	v_pk_add_f32 v[26:27], v[26:27], v[34:35]
	s_nop 1
	v_mov_b32_dpp v28, v26 quad_perm:[2,3,0,1] row_mask:0xf bank_mask:0xf
	v_mov_b32_dpp v29, v27 quad_perm:[2,3,0,1] row_mask:0xf bank_mask:0xf
	v_mul_lo_u32 v24, v25, s30
	v_add_lshl_u32 v24, v31, v24, 1
	v_cvt_pk_f16_f32 v38, v49, v40
	buffer_store_dwordx4 v[36:39], v24, s[8:11], 0 offen sc1
	s_waitcnt lgkmcnt(0)
	v_pk_add_f32 v[26:27], v[26:27], v[28:29]
	s_lshl_b32 s2, s15, 4
	v_mov_b32_e32 v24, v7
	s_nop 1
	v_mov_b32_dpp v28, v26 quad_perm:[1,0,3,2] row_mask:0xf bank_mask:0xf
	v_mov_b32_dpp v29, v27 quad_perm:[1,0,3,2] row_mask:0xf bank_mask:0xf
	s_and_saveexec_b64 s[0:1], vcc
	s_cbranch_execz .LBB7_5
	s_waitcnt lgkmcnt(0)
	v_pk_add_f32 v[64:65], v[26:27], v[28:29]
	v_lshl_add_u32 v23, v25, 6, s2
	v_mov_b32_e32 v67, v66
	s_mov_b32 s18, s10
	s_mov_b32 s19, s11
	buffer_store_dwordx4 v[64:67], v23, s[16:19], 0 offen sc1

.LBB9_3:
	s_ashr_i32 s44, s23, 31
	s_xor_b32 s44, s44, s25
	s_abs_i32 s45, s23
	s_mul_hi_u32 s48, s45, s26
	s_mul_i32 s49, s48, s24
	s_sub_i32 s45, s45, s49
	s_add_i32 s49, s48, 1
	s_sub_i32 s46, s45, s24
	s_cmp_ge_u32 s45, s24
	s_cselect_b32 s48, s49, s48
	s_cselect_b32 s45, s46, s45
	s_add_i32 s49, s48, 1
	s_cmp_ge_u32 s45, s24
	s_cselect_b32 s45, s49, s48
	s_xor_b32 s45, s45, s44
	s_sub_i32 s44, s45, s44
	s_mul_i32 s45, s44, s21
	s_sub_i32 s47, s23, s45
	s_lshl_b32 s48, s47, 7
	s_lshl_b32 s46, s44, 7
	s_ashr_i32 s49, s48, 31
	v_or_b32_e32 v152, s46, v1
	v_lshl_add_u64 v[154:155], s[48:49], 1, v[70:71]
	v_mad_i64_i32 v[156:157], s[50:51], v152, s29, v[154:155]
	v_lshl_add_u64 v[158:159], s[48:49], 2, v[68:69]
	v_or_b32_e32 v153, 32, v152
	global_load_dwordx4 v[160:163], v[156:157], off
	v_mad_i64_i32 v[184:185], s[50:51], v153, s29, v[154:155]
	v_or_b32_e32 v153, 64, v152
	global_load_dwordx4 v[176:179], v[158:159], off
	global_load_dwordx4 v[180:183], v[158:159], off offset:16
	v_mad_i64_i32 v[186:187], s[50:51], v153, s29, v[154:155]
	v_or_b32_e32 v153, 0x60, v152
	global_load_dwordx4 v[164:167], v[184:185], off
	v_mad_i64_i32 v[188:189], s[50:51], v153, s29, v[154:155]
	global_load_dwordx4 v[168:171], v[186:187], off
	s_nop 0
	global_load_dwordx4 v[172:175], v[188:189], off
	v_add_u32_e32 v110, v80, v76
	s_waitcnt vmcnt(14)
	s_barrier
	s_waitcnt lgkmcnt(0)
	ds_read_b128 v[2:5], v110 offset:16384
	v_add_u32_e32 v111, v79, v76
	ds_read_b128 v[6:9], v111
	ds_read_b128 v[10:13], v111 offset:4096
	ds_read_b128 v[14:17], v110 offset:20480
	v_add_u32_e32 v67, v80, v77
	ds_read_b128 v[34:37], v67 offset:16384
	v_add_u32_e32 v109, v79, v77
	s_waitcnt lgkmcnt(3)
	v_mfma_f32_32x32x16_f16 v[50:65], v[2:5], v[6:9], 0
	ds_read_b128 v[112:115], v109
	ds_read_b128 v[116:119], v109 offset:4096
	ds_read_b128 v[120:123], v67 offset:20480
	v_readfirstlane_b32 s2, v0
	s_lshl_b32 s35, s27, 15
	s_lshl_b32 s2, s2, 4
	s_add_i32 s1, s35, 0
	s_and_b32 s39, s2, 0xfffffc00
	s_add_i32 s1, s1, s39
	s_waitcnt lgkmcnt(5)
	v_mfma_f32_32x32x16_f16 v[18:33], v[2:5], v[10:13], 0
	s_mov_b32 m0, s1
	s_add_i32 s2, s1, 0x2000
	buffer_load_dwordx4 v72, s[4:7], s0 offen lds
	s_mov_b32 m0, s2
	s_add_i32 s3, s1, 0x4000
	buffer_load_dwordx4 v74, s[4:7], s0 offen lds
	s_mov_b32 s14, s10
	s_waitcnt lgkmcnt(2)
	v_mfma_f32_32x32x16_f16 v[50:65], v[34:37], v[112:115], v[50:65]
	s_mov_b32 s15, s11
	s_mov_b32 m0, s3
	s_add_i32 s18, s1, 0x6000
	buffer_load_dwordx4 v73, s[12:15], s0 offen lds
	s_mov_b32 m0, s18
	s_add_i32 s19, s35, 0x8000
	buffer_load_dwordx4 v75, s[12:15], s0 offen lds
	s_waitcnt lgkmcnt(1)
	v_mfma_f32_32x32x16_f16 v[18:33], v[34:37], v[116:119], v[18:33]
	s_waitcnt vmcnt(14)
	s_barrier
	s_and_b32 s19, s19, 0x18000
	s_add_i32 s19, s19, 0
	s_add_i32 s19, s19, s39
	s_add_i32 s36, s0, 0x80
	s_mov_b32 m0, s19
	v_mfma_f32_32x32x16_f16 v[34:49], v[14:17], v[6:9], 0
	s_add_i32 s31, s19, 0x2000
	s_add_i32 s33, s19, 0x4000
	s_add_i32 s34, s19, 0x6000
	s_xor_b32 s40, s35, 0x10000
	s_add_i32 s35, s40, 0
	s_add_i32 s35, s35, s39
	s_add_i32 s41, s0, 0x100
	v_mfma_f32_32x32x16_f16 v[2:17], v[14:17], v[10:13], 0
	s_add_i32 s37, s35, 0x4000
	s_add_i32 s38, s35, 0x6000
	s_add_i32 s40, s40, 0x8000
	s_and_b32 s40, s40, 0x18000
	s_add_i32 s40, s40, 0
	s_add_i32 s39, s40, s39
	s_add_i32 s43, s0, 0x180
	s_waitcnt lgkmcnt(0)
	v_mfma_f32_32x32x16_f16 v[34:49], v[120:123], v[112:115], v[34:49]
	s_add_i32 s40, s39, 0x2000
	s_add_i32 s42, s39, 0x6000
	v_mfma_f32_32x32x16_f16 v[2:17], v[120:123], v[116:119], v[2:17]
	ds_read_b128 v[112:115], v110 offset:49152
	ds_read_b128 v[116:119], v111 offset:32768
	ds_read_b128 v[120:123], v111 offset:36864
	ds_read_b128 v[124:127], v110 offset:53248
	s_waitcnt lgkmcnt(2)
	v_mfma_f32_32x32x16_f16 v[50:65], v[112:115], v[116:119], v[50:65]
	s_waitcnt lgkmcnt(1)
	v_mfma_f32_32x32x16_f16 v[18:33], v[112:115], v[120:123], v[18:33]
	s_waitcnt lgkmcnt(0)
	v_mfma_f32_32x32x16_f16 v[34:49], v[124:127], v[116:119], v[34:49]
	v_mfma_f32_32x32x16_f16 v[2:17], v[124:127], v[120:123], v[2:17]
	ds_read_b128 v[112:115], v67 offset:49152
	ds_read_b128 v[116:119], v109 offset:32768
	ds_read_b128 v[120:123], v109 offset:36864
	ds_read_b128 v[124:127], v67 offset:53248
	buffer_load_dwordx4 v72, s[4:7], s36 offen lds
	s_mov_b32 m0, s31
	s_nop 0
	buffer_load_dwordx4 v74, s[4:7], s36 offen lds
	s_mov_b32 m0, s33
	s_nop 0
	buffer_load_dwordx4 v73, s[12:15], s36 offen lds
	s_mov_b32 m0, s34
	s_waitcnt lgkmcnt(2)
	v_mfma_f32_32x32x16_f16 v[50:65], v[112:115], v[116:119], v[50:65]
	buffer_load_dwordx4 v75, s[12:15], s36 offen lds
	s_waitcnt vmcnt(14)
	s_barrier
	s_mov_b32 m0, s35
	s_add_i32 s36, s35, 0x2000
	s_waitcnt lgkmcnt(1)
	v_mfma_f32_32x32x16_f16 v[18:33], v[112:115], v[120:123], v[18:33]
	v_add_u32_e32 v113, v81, v76
	v_add_u32_e32 v112, v82, v76
	s_waitcnt lgkmcnt(0)
	v_mfma_f32_32x32x16_f16 v[34:49], v[124:127], v[116:119], v[34:49]
	ds_read_b128 v[114:117], v96
	v_mfma_f32_32x32x16_f16 v[2:17], v[124:127], v[120:123], v[2:17]
	ds_read_b128 v[118:121], v113
	ds_read_b128 v[122:125], v113 offset:4096
	ds_read_b128 v[126:129], v112 offset:4096
	s_waitcnt lgkmcnt(2)
	v_mfma_f32_32x32x16_f16 v[50:65], v[114:117], v[118:121], v[50:65]
	s_waitcnt lgkmcnt(1)
	v_mfma_f32_32x32x16_f16 v[18:33], v[114:117], v[122:125], v[18:33]
	v_add_u32_e32 v115, v81, v77
	v_add_u32_e32 v114, v82, v77
	s_waitcnt lgkmcnt(0)
	v_mfma_f32_32x32x16_f16 v[34:49], v[126:129], v[118:121], v[34:49]
	ds_read_b128 v[116:119], v97
	v_mfma_f32_32x32x16_f16 v[2:17], v[126:129], v[122:125], v[2:17]
	ds_read_b128 v[120:123], v115
	ds_read_b128 v[124:127], v115 offset:4096
	ds_read_b128 v[128:131], v114 offset:4096
	buffer_load_dwordx4 v72, s[4:7], s41 offen lds
	s_mov_b32 m0, s36
	s_nop 0
	buffer_load_dwordx4 v74, s[4:7], s41 offen lds
	s_mov_b32 m0, s37
	s_waitcnt lgkmcnt(2)
	v_mfma_f32_32x32x16_f16 v[50:65], v[116:119], v[120:123], v[50:65]
	buffer_load_dwordx4 v73, s[12:15], s41 offen lds
	s_mov_b32 m0, s38
	s_nop 0
	buffer_load_dwordx4 v75, s[12:15], s41 offen lds
	s_waitcnt vmcnt(8)
	s_barrier
	s_mov_b32 m0, s39
	s_waitcnt lgkmcnt(1)
	v_mfma_f32_32x32x16_f16 v[18:33], v[116:119], v[124:127], v[18:33]
	v_add_u32_e32 v117, v83, v76
	v_add_u32_e32 v116, v84, v76
	s_add_i32 s41, s39, 0x4000
	s_waitcnt lgkmcnt(0)
	v_mfma_f32_32x32x16_f16 v[34:49], v[128:131], v[120:123], v[34:49]
	ds_read_b128 v[118:121], v98
	v_mfma_f32_32x32x16_f16 v[2:17], v[128:131], v[124:127], v[2:17]
	ds_read_b128 v[122:125], v117
	ds_read_b128 v[126:129], v117 offset:4096
	ds_read_b128 v[130:133], v116 offset:4096
	s_waitcnt lgkmcnt(2)
	v_mfma_f32_32x32x16_f16 v[50:65], v[118:121], v[122:125], v[50:65]
	s_waitcnt lgkmcnt(1)
	v_mfma_f32_32x32x16_f16 v[18:33], v[118:121], v[126:129], v[18:33]
	v_add_u32_e32 v119, v83, v77
	v_add_u32_e32 v118, v84, v77
	s_waitcnt lgkmcnt(0)
	v_mfma_f32_32x32x16_f16 v[34:49], v[130:133], v[122:125], v[34:49]
	ds_read_b128 v[120:123], v99
	v_mfma_f32_32x32x16_f16 v[2:17], v[130:133], v[126:129], v[2:17]
	ds_read_b128 v[124:127], v119
	ds_read_b128 v[128:131], v119 offset:4096
	ds_read_b128 v[132:135], v118 offset:4096
	buffer_load_dwordx4 v72, s[4:7], s43 offen lds
	s_mov_b32 m0, s40
	s_nop 0
	buffer_load_dwordx4 v74, s[4:7], s43 offen lds
	s_mov_b32 m0, s41
	s_waitcnt lgkmcnt(2)
	v_mfma_f32_32x32x16_f16 v[50:65], v[120:123], v[124:127], v[50:65]
	buffer_load_dwordx4 v73, s[12:15], s43 offen lds
	s_mov_b32 m0, s42
	s_nop 0
	buffer_load_dwordx4 v75, s[12:15], s43 offen lds
	s_waitcnt vmcnt(8)
	s_barrier
	s_add_i32 s43, s0, 0x200
	s_waitcnt lgkmcnt(1)
	v_mfma_f32_32x32x16_f16 v[18:33], v[120:123], v[128:131], v[18:33]
	s_mov_b32 m0, s1
	s_waitcnt lgkmcnt(0)
	v_mfma_f32_32x32x16_f16 v[34:49], v[132:135], v[124:127], v[34:49]
	v_mfma_f32_32x32x16_f16 v[2:17], v[132:135], v[128:131], v[2:17]
	ds_read_b128 v[120:123], v110 offset:16384
	ds_read_b128 v[124:127], v111
	ds_read_b128 v[128:131], v111 offset:4096
	ds_read_b128 v[132:135], v110 offset:20480
	s_waitcnt lgkmcnt(2)
	v_mfma_f32_32x32x16_f16 v[50:65], v[120:123], v[124:127], v[50:65]
	s_waitcnt lgkmcnt(1)
	v_mfma_f32_32x32x16_f16 v[18:33], v[120:123], v[128:131], v[18:33]
	s_waitcnt lgkmcnt(0)
	v_mfma_f32_32x32x16_f16 v[34:49], v[132:135], v[124:127], v[34:49]
	v_mfma_f32_32x32x16_f16 v[2:17], v[132:135], v[128:131], v[2:17]
	ds_read_b128 v[120:123], v67 offset:16384
	ds_read_b128 v[124:127], v109
	ds_read_b128 v[128:131], v109 offset:4096
	ds_read_b128 v[132:135], v67 offset:20480
	buffer_load_dwordx4 v72, s[4:7], s43 offen lds
	s_mov_b32 m0, s2
	s_nop 0
	buffer_load_dwordx4 v74, s[4:7], s43 offen lds
	s_mov_b32 m0, s3
	s_waitcnt lgkmcnt(2)
	v_mfma_f32_32x32x16_f16 v[50:65], v[120:123], v[124:127], v[50:65]
	buffer_load_dwordx4 v73, s[12:15], s43 offen lds
	s_mov_b32 m0, s18
	s_nop 0
	buffer_load_dwordx4 v75, s[12:15], s43 offen lds
	s_waitcnt vmcnt(8)
	s_barrier
	s_add_i32 s43, s0, 0x280
	s_waitcnt lgkmcnt(1)
	v_mfma_f32_32x32x16_f16 v[18:33], v[120:123], v[128:131], v[18:33]
	s_mov_b32 m0, s19
	s_waitcnt lgkmcnt(0)
	v_mfma_f32_32x32x16_f16 v[34:49], v[132:135], v[124:127], v[34:49]
	v_mfma_f32_32x32x16_f16 v[2:17], v[132:135], v[128:131], v[2:17]
	ds_read_b128 v[120:123], v110 offset:49152
	ds_read_b128 v[124:127], v111 offset:32768
	ds_read_b128 v[128:131], v111 offset:36864
	ds_read_b128 v[132:135], v110 offset:53248
	s_waitcnt lgkmcnt(2)
	v_mfma_f32_32x32x16_f16 v[50:65], v[120:123], v[124:127], v[50:65]
	s_waitcnt lgkmcnt(1)
	v_mfma_f32_32x32x16_f16 v[18:33], v[120:123], v[128:131], v[18:33]
	s_waitcnt lgkmcnt(0)
	v_mfma_f32_32x32x16_f16 v[34:49], v[132:135], v[124:127], v[34:49]
	v_mfma_f32_32x32x16_f16 v[2:17], v[132:135], v[128:131], v[2:17]
	ds_read_b128 v[120:123], v67 offset:49152
	ds_read_b128 v[124:127], v109 offset:32768
	ds_read_b128 v[128:131], v109 offset:36864
	ds_read_b128 v[132:135], v67 offset:53248
	buffer_load_dwordx4 v72, s[4:7], s43 offen lds
	s_mov_b32 m0, s31
	s_nop 0
	buffer_load_dwordx4 v74, s[4:7], s43 offen lds
	s_mov_b32 m0, s33
	s_waitcnt lgkmcnt(2)
	v_mfma_f32_32x32x16_f16 v[50:65], v[120:123], v[124:127], v[50:65]
	buffer_load_dwordx4 v73, s[12:15], s43 offen lds
	s_mov_b32 m0, s34
	s_nop 0
	buffer_load_dwordx4 v75, s[12:15], s43 offen lds
	s_waitcnt vmcnt(8)
	s_barrier
	s_add_i32 s43, s0, 0x300
	s_waitcnt lgkmcnt(1)
	v_mfma_f32_32x32x16_f16 v[18:33], v[120:123], v[128:131], v[18:33]
	s_mov_b32 m0, s35
	s_waitcnt lgkmcnt(0)
	v_mfma_f32_32x32x16_f16 v[34:49], v[132:135], v[124:127], v[34:49]
	v_mfma_f32_32x32x16_f16 v[2:17], v[132:135], v[128:131], v[2:17]
	ds_read_b128 v[120:123], v96
	ds_read_b128 v[124:127], v113
	ds_read_b128 v[128:131], v113 offset:4096
	ds_read_b128 v[132:135], v112 offset:4096
	s_waitcnt lgkmcnt(2)
	v_mfma_f32_32x32x16_f16 v[50:65], v[120:123], v[124:127], v[50:65]
	s_waitcnt lgkmcnt(1)
	v_mfma_f32_32x32x16_f16 v[18:33], v[120:123], v[128:131], v[18:33]
	s_waitcnt lgkmcnt(0)
	v_mfma_f32_32x32x16_f16 v[34:49], v[132:135], v[124:127], v[34:49]
	v_mfma_f32_32x32x16_f16 v[2:17], v[132:135], v[128:131], v[2:17]
	ds_read_b128 v[120:123], v97
	ds_read_b128 v[124:127], v115
	ds_read_b128 v[128:131], v115 offset:4096
	ds_read_b128 v[132:135], v114 offset:4096
	buffer_load_dwordx4 v72, s[4:7], s43 offen lds
	s_mov_b32 m0, s36
	s_nop 0
	buffer_load_dwordx4 v74, s[4:7], s43 offen lds
	s_mov_b32 m0, s37
	s_waitcnt lgkmcnt(2)
	v_mfma_f32_32x32x16_f16 v[50:65], v[120:123], v[124:127], v[50:65]
	buffer_load_dwordx4 v73, s[12:15], s43 offen lds
	s_mov_b32 m0, s38
	s_nop 0
	buffer_load_dwordx4 v75, s[12:15], s43 offen lds
	s_waitcnt vmcnt(8)
	s_barrier
	s_add_i32 s43, s0, 0x380
	s_waitcnt lgkmcnt(1)
	v_mfma_f32_32x32x16_f16 v[18:33], v[120:123], v[128:131], v[18:33]
	s_mov_b32 m0, s39
	s_waitcnt lgkmcnt(0)
	v_mfma_f32_32x32x16_f16 v[34:49], v[132:135], v[124:127], v[34:49]
	v_mfma_f32_32x32x16_f16 v[2:17], v[132:135], v[128:131], v[2:17]
	ds_read_b128 v[120:123], v98
	ds_read_b128 v[124:127], v117
	ds_read_b128 v[128:131], v117 offset:4096
	ds_read_b128 v[132:135], v116 offset:4096
	s_waitcnt lgkmcnt(2)
	v_mfma_f32_32x32x16_f16 v[50:65], v[120:123], v[124:127], v[50:65]
	s_waitcnt lgkmcnt(1)
	v_mfma_f32_32x32x16_f16 v[18:33], v[120:123], v[128:131], v[18:33]
	s_waitcnt lgkmcnt(0)
	v_mfma_f32_32x32x16_f16 v[34:49], v[132:135], v[124:127], v[34:49]
	v_mfma_f32_32x32x16_f16 v[2:17], v[132:135], v[128:131], v[2:17]
	ds_read_b128 v[120:123], v99
	ds_read_b128 v[124:127], v119
	ds_read_b128 v[128:131], v119 offset:4096
	ds_read_b128 v[132:135], v118 offset:4096
	buffer_load_dwordx4 v72, s[4:7], s43 offen lds
	s_mov_b32 m0, s40
	s_nop 0
	buffer_load_dwordx4 v74, s[4:7], s43 offen lds
	s_mov_b32 m0, s41
	s_waitcnt lgkmcnt(2)
	v_mfma_f32_32x32x16_f16 v[50:65], v[120:123], v[124:127], v[50:65]
	buffer_load_dwordx4 v73, s[12:15], s43 offen lds
	s_mov_b32 m0, s42
	s_nop 0
	buffer_load_dwordx4 v75, s[12:15], s43 offen lds
	s_waitcnt vmcnt(8)
	s_barrier
	s_add_i32 s43, s0, 0x400
	s_waitcnt lgkmcnt(1)
	v_mfma_f32_32x32x16_f16 v[18:33], v[120:123], v[128:131], v[18:33]
	s_mov_b32 m0, s1
	s_waitcnt lgkmcnt(0)
	v_mfma_f32_32x32x16_f16 v[34:49], v[132:135], v[124:127], v[34:49]
	v_mfma_f32_32x32x16_f16 v[2:17], v[132:135], v[128:131], v[2:17]
	ds_read_b128 v[120:123], v110 offset:16384
	ds_read_b128 v[124:127], v111
	ds_read_b128 v[128:131], v111 offset:4096
	ds_read_b128 v[132:135], v110 offset:20480
	s_waitcnt lgkmcnt(2)
	v_mfma_f32_32x32x16_f16 v[50:65], v[120:123], v[124:127], v[50:65]
	s_waitcnt lgkmcnt(1)
	v_mfma_f32_32x32x16_f16 v[18:33], v[120:123], v[128:131], v[18:33]
	s_waitcnt lgkmcnt(0)
	v_mfma_f32_32x32x16_f16 v[34:49], v[132:135], v[124:127], v[34:49]
	v_mfma_f32_32x32x16_f16 v[2:17], v[132:135], v[128:131], v[2:17]
	ds_read_b128 v[120:123], v67 offset:16384
	ds_read_b128 v[124:127], v109
	ds_read_b128 v[128:131], v109 offset:4096
	ds_read_b128 v[132:135], v67 offset:20480
	buffer_load_dwordx4 v72, s[4:7], s43 offen lds
	s_mov_b32 m0, s2
	s_nop 0
	buffer_load_dwordx4 v74, s[4:7], s43 offen lds
	s_mov_b32 m0, s3
	s_waitcnt lgkmcnt(2)
	v_mfma_f32_32x32x16_f16 v[50:65], v[120:123], v[124:127], v[50:65]
	buffer_load_dwordx4 v73, s[12:15], s43 offen lds
	s_mov_b32 m0, s18
	s_nop 0
	buffer_load_dwordx4 v75, s[12:15], s43 offen lds
	s_waitcnt vmcnt(8)
	s_barrier
	s_add_i32 s43, s0, 0x480
	s_waitcnt lgkmcnt(1)
	v_mfma_f32_32x32x16_f16 v[18:33], v[120:123], v[128:131], v[18:33]
	s_mov_b32 m0, s19
	s_waitcnt lgkmcnt(0)
	v_mfma_f32_32x32x16_f16 v[34:49], v[132:135], v[124:127], v[34:49]
	v_mfma_f32_32x32x16_f16 v[2:17], v[132:135], v[128:131], v[2:17]
	ds_read_b128 v[120:123], v110 offset:49152
	ds_read_b128 v[124:127], v111 offset:32768
	ds_read_b128 v[128:131], v111 offset:36864
	ds_read_b128 v[132:135], v110 offset:53248
	s_waitcnt lgkmcnt(2)
	v_mfma_f32_32x32x16_f16 v[50:65], v[120:123], v[124:127], v[50:65]
	s_waitcnt lgkmcnt(1)
	v_mfma_f32_32x32x16_f16 v[18:33], v[120:123], v[128:131], v[18:33]
	s_waitcnt lgkmcnt(0)
	v_mfma_f32_32x32x16_f16 v[34:49], v[132:135], v[124:127], v[34:49]
	v_mfma_f32_32x32x16_f16 v[2:17], v[132:135], v[128:131], v[2:17]
	ds_read_b128 v[120:123], v67 offset:49152
	ds_read_b128 v[124:127], v109 offset:32768
	ds_read_b128 v[128:131], v109 offset:36864
	ds_read_b128 v[132:135], v67 offset:53248
	buffer_load_dwordx4 v72, s[4:7], s43 offen lds
	s_mov_b32 m0, s31
	s_nop 0
	buffer_load_dwordx4 v74, s[4:7], s43 offen lds
	s_mov_b32 m0, s33
	s_waitcnt lgkmcnt(2)
	v_mfma_f32_32x32x16_f16 v[50:65], v[120:123], v[124:127], v[50:65]
	buffer_load_dwordx4 v73, s[12:15], s43 offen lds
	s_mov_b32 m0, s34
	s_nop 0
	buffer_load_dwordx4 v75, s[12:15], s43 offen lds
	s_waitcnt vmcnt(8)
	s_barrier
	s_add_i32 s43, s0, 0x500
	s_waitcnt lgkmcnt(1)
	v_mfma_f32_32x32x16_f16 v[18:33], v[120:123], v[128:131], v[18:33]
	s_mov_b32 m0, s35
	s_waitcnt lgkmcnt(0)
	v_mfma_f32_32x32x16_f16 v[34:49], v[132:135], v[124:127], v[34:49]
	v_mfma_f32_32x32x16_f16 v[2:17], v[132:135], v[128:131], v[2:17]
	ds_read_b128 v[120:123], v96
	ds_read_b128 v[124:127], v113
	ds_read_b128 v[128:131], v113 offset:4096
	ds_read_b128 v[132:135], v112 offset:4096
	s_waitcnt lgkmcnt(2)
	v_mfma_f32_32x32x16_f16 v[50:65], v[120:123], v[124:127], v[50:65]
	s_waitcnt lgkmcnt(1)
	v_mfma_f32_32x32x16_f16 v[18:33], v[120:123], v[128:131], v[18:33]
	s_waitcnt lgkmcnt(0)
	v_mfma_f32_32x32x16_f16 v[34:49], v[132:135], v[124:127], v[34:49]
	v_mfma_f32_32x32x16_f16 v[2:17], v[132:135], v[128:131], v[2:17]
	ds_read_b128 v[120:123], v97
	ds_read_b128 v[124:127], v115
	ds_read_b128 v[128:131], v115 offset:4096
	ds_read_b128 v[132:135], v114 offset:4096
	buffer_load_dwordx4 v72, s[4:7], s43 offen lds
	s_mov_b32 m0, s36
	s_nop 0
	buffer_load_dwordx4 v74, s[4:7], s43 offen lds
	s_mov_b32 m0, s37
	s_waitcnt lgkmcnt(2)
	v_mfma_f32_32x32x16_f16 v[50:65], v[120:123], v[124:127], v[50:65]
	buffer_load_dwordx4 v73, s[12:15], s43 offen lds
	s_mov_b32 m0, s38
	s_nop 0
	buffer_load_dwordx4 v75, s[12:15], s43 offen lds
	s_waitcnt vmcnt(8)
	s_barrier
	s_add_i32 s43, s0, 0x580
	s_waitcnt lgkmcnt(1)
	v_mfma_f32_32x32x16_f16 v[18:33], v[120:123], v[128:131], v[18:33]
	s_mov_b32 m0, s39
	s_waitcnt lgkmcnt(0)
	v_mfma_f32_32x32x16_f16 v[34:49], v[132:135], v[124:127], v[34:49]
	v_mfma_f32_32x32x16_f16 v[2:17], v[132:135], v[128:131], v[2:17]
	ds_read_b128 v[120:123], v98
	ds_read_b128 v[124:127], v117
	ds_read_b128 v[128:131], v117 offset:4096
	ds_read_b128 v[132:135], v116 offset:4096
	s_waitcnt lgkmcnt(2)
	v_mfma_f32_32x32x16_f16 v[50:65], v[120:123], v[124:127], v[50:65]
	s_waitcnt lgkmcnt(1)
	v_mfma_f32_32x32x16_f16 v[18:33], v[120:123], v[128:131], v[18:33]
	s_waitcnt lgkmcnt(0)
	v_mfma_f32_32x32x16_f16 v[34:49], v[132:135], v[124:127], v[34:49]
	v_mfma_f32_32x32x16_f16 v[2:17], v[132:135], v[128:131], v[2:17]
	ds_read_b128 v[120:123], v99
	ds_read_b128 v[124:127], v119
	ds_read_b128 v[128:131], v119 offset:4096
	ds_read_b128 v[132:135], v118 offset:4096
	buffer_load_dwordx4 v72, s[4:7], s43 offen lds
	s_mov_b32 m0, s40
	s_nop 0
	buffer_load_dwordx4 v74, s[4:7], s43 offen lds
	s_mov_b32 m0, s41
	s_waitcnt lgkmcnt(2)
	v_mfma_f32_32x32x16_f16 v[50:65], v[120:123], v[124:127], v[50:65]
	buffer_load_dwordx4 v73, s[12:15], s43 offen lds
	s_mov_b32 m0, s42
	s_nop 0
	buffer_load_dwordx4 v75, s[12:15], s43 offen lds
	s_waitcnt vmcnt(8)
	s_barrier
	s_add_i32 s43, s0, 0x600
	s_waitcnt lgkmcnt(1)
	v_mfma_f32_32x32x16_f16 v[18:33], v[120:123], v[128:131], v[18:33]
	s_mov_b32 m0, s1
	s_waitcnt lgkmcnt(0)
	v_mfma_f32_32x32x16_f16 v[34:49], v[132:135], v[124:127], v[34:49]
	v_mfma_f32_32x32x16_f16 v[2:17], v[132:135], v[128:131], v[2:17]
	ds_read_b128 v[120:123], v110 offset:16384
	ds_read_b128 v[124:127], v111
	ds_read_b128 v[128:131], v111 offset:4096
	ds_read_b128 v[132:135], v110 offset:20480
	s_waitcnt lgkmcnt(2)
	v_mfma_f32_32x32x16_f16 v[50:65], v[120:123], v[124:127], v[50:65]
	s_waitcnt lgkmcnt(1)
	v_mfma_f32_32x32x16_f16 v[18:33], v[120:123], v[128:131], v[18:33]
	s_waitcnt lgkmcnt(0)
	v_mfma_f32_32x32x16_f16 v[34:49], v[132:135], v[124:127], v[34:49]
	v_mfma_f32_32x32x16_f16 v[2:17], v[132:135], v[128:131], v[2:17]
	ds_read_b128 v[120:123], v67 offset:16384
	ds_read_b128 v[124:127], v109
	ds_read_b128 v[128:131], v109 offset:4096
	ds_read_b128 v[132:135], v67 offset:20480
	buffer_load_dwordx4 v72, s[4:7], s43 offen lds
	s_mov_b32 m0, s2
	s_nop 0
	buffer_load_dwordx4 v74, s[4:7], s43 offen lds
	s_mov_b32 m0, s3
	s_waitcnt lgkmcnt(2)
	v_mfma_f32_32x32x16_f16 v[50:65], v[120:123], v[124:127], v[50:65]
	buffer_load_dwordx4 v73, s[12:15], s43 offen lds
	s_mov_b32 m0, s18
	s_nop 0
	buffer_load_dwordx4 v75, s[12:15], s43 offen lds
	s_waitcnt vmcnt(8)
	s_barrier
	s_add_i32 s43, s0, 0x680
	s_waitcnt lgkmcnt(1)
	v_mfma_f32_32x32x16_f16 v[18:33], v[120:123], v[128:131], v[18:33]
	s_mov_b32 m0, s19
	s_waitcnt lgkmcnt(0)
	v_mfma_f32_32x32x16_f16 v[34:49], v[132:135], v[124:127], v[34:49]
	v_mfma_f32_32x32x16_f16 v[2:17], v[132:135], v[128:131], v[2:17]
	ds_read_b128 v[120:123], v110 offset:49152
	ds_read_b128 v[124:127], v111 offset:32768
	ds_read_b128 v[128:131], v111 offset:36864
	ds_read_b128 v[132:135], v110 offset:53248
	s_waitcnt lgkmcnt(2)
	v_mfma_f32_32x32x16_f16 v[50:65], v[120:123], v[124:127], v[50:65]
	s_waitcnt lgkmcnt(1)
	v_mfma_f32_32x32x16_f16 v[18:33], v[120:123], v[128:131], v[18:33]
	s_waitcnt lgkmcnt(0)
	v_mfma_f32_32x32x16_f16 v[34:49], v[132:135], v[124:127], v[34:49]
	v_mfma_f32_32x32x16_f16 v[2:17], v[132:135], v[128:131], v[2:17]
	ds_read_b128 v[120:123], v67 offset:49152
	ds_read_b128 v[124:127], v109 offset:32768
	ds_read_b128 v[128:131], v109 offset:36864
	ds_read_b128 v[132:135], v67 offset:53248
	buffer_load_dwordx4 v72, s[4:7], s43 offen lds
	s_mov_b32 m0, s31
	s_nop 0
	buffer_load_dwordx4 v74, s[4:7], s43 offen lds
	s_mov_b32 m0, s33
	s_waitcnt lgkmcnt(2)
	v_mfma_f32_32x32x16_f16 v[50:65], v[120:123], v[124:127], v[50:65]
	buffer_load_dwordx4 v73, s[12:15], s43 offen lds
	s_mov_b32 m0, s34
	s_nop 0
	buffer_load_dwordx4 v75, s[12:15], s43 offen lds
	s_waitcnt vmcnt(8)
	s_barrier
	s_add_i32 s43, s0, 0x700
	s_waitcnt lgkmcnt(1)
	v_mfma_f32_32x32x16_f16 v[18:33], v[120:123], v[128:131], v[18:33]
	s_mov_b32 m0, s35
	s_waitcnt lgkmcnt(0)
	v_mfma_f32_32x32x16_f16 v[34:49], v[132:135], v[124:127], v[34:49]
	v_mfma_f32_32x32x16_f16 v[2:17], v[132:135], v[128:131], v[2:17]
	ds_read_b128 v[120:123], v96
	ds_read_b128 v[124:127], v113
	ds_read_b128 v[128:131], v113 offset:4096
	ds_read_b128 v[132:135], v112 offset:4096
	s_waitcnt lgkmcnt(2)
	v_mfma_f32_32x32x16_f16 v[50:65], v[120:123], v[124:127], v[50:65]
	s_waitcnt lgkmcnt(1)
	v_mfma_f32_32x32x16_f16 v[18:33], v[120:123], v[128:131], v[18:33]
	s_waitcnt lgkmcnt(0)
	v_mfma_f32_32x32x16_f16 v[34:49], v[132:135], v[124:127], v[34:49]
	v_mfma_f32_32x32x16_f16 v[2:17], v[132:135], v[128:131], v[2:17]
	ds_read_b128 v[120:123], v97
	ds_read_b128 v[124:127], v115
	ds_read_b128 v[128:131], v115 offset:4096
	ds_read_b128 v[132:135], v114 offset:4096
	buffer_load_dwordx4 v72, s[4:7], s43 offen lds
	s_mov_b32 m0, s36
	s_nop 0
	buffer_load_dwordx4 v74, s[4:7], s43 offen lds
	s_mov_b32 m0, s37
	s_waitcnt lgkmcnt(2)
	v_mfma_f32_32x32x16_f16 v[50:65], v[120:123], v[124:127], v[50:65]
	buffer_load_dwordx4 v73, s[12:15], s43 offen lds
	s_mov_b32 m0, s38
	s_nop 0
	buffer_load_dwordx4 v75, s[12:15], s43 offen lds
	s_waitcnt vmcnt(8)
	s_barrier
	s_add_i32 s43, s0, 0x780
	s_waitcnt lgkmcnt(1)
	v_mfma_f32_32x32x16_f16 v[18:33], v[120:123], v[128:131], v[18:33]
	s_mov_b32 m0, s39
	s_waitcnt lgkmcnt(0)
	v_mfma_f32_32x32x16_f16 v[34:49], v[132:135], v[124:127], v[34:49]
	v_mfma_f32_32x32x16_f16 v[2:17], v[132:135], v[128:131], v[2:17]
	ds_read_b128 v[120:123], v98
	ds_read_b128 v[124:127], v117
	ds_read_b128 v[128:131], v117 offset:4096
	ds_read_b128 v[132:135], v116 offset:4096
	s_waitcnt lgkmcnt(2)
	v_mfma_f32_32x32x16_f16 v[50:65], v[120:123], v[124:127], v[50:65]
	s_waitcnt lgkmcnt(1)
	v_mfma_f32_32x32x16_f16 v[18:33], v[120:123], v[128:131], v[18:33]
	s_waitcnt lgkmcnt(0)
	v_mfma_f32_32x32x16_f16 v[34:49], v[132:135], v[124:127], v[34:49]
	v_mfma_f32_32x32x16_f16 v[2:17], v[132:135], v[128:131], v[2:17]
	ds_read_b128 v[120:123], v99
	ds_read_b128 v[124:127], v119
	ds_read_b128 v[128:131], v119 offset:4096
	ds_read_b128 v[132:135], v118 offset:4096
	buffer_load_dwordx4 v72, s[4:7], s43 offen lds
	s_mov_b32 m0, s40
	s_nop 0
	buffer_load_dwordx4 v74, s[4:7], s43 offen lds
	s_mov_b32 m0, s41
	s_waitcnt lgkmcnt(2)
	v_mfma_f32_32x32x16_f16 v[50:65], v[120:123], v[124:127], v[50:65]
	buffer_load_dwordx4 v73, s[12:15], s43 offen lds
	s_mov_b32 m0, s42
	s_nop 0
	buffer_load_dwordx4 v75, s[12:15], s43 offen lds
	s_waitcnt vmcnt(8)
	s_barrier
	s_add_i32 s43, s0, 0x800
	s_waitcnt lgkmcnt(1)
	v_mfma_f32_32x32x16_f16 v[18:33], v[120:123], v[128:131], v[18:33]
	s_mov_b32 m0, s1
	s_waitcnt lgkmcnt(0)
	v_mfma_f32_32x32x16_f16 v[34:49], v[132:135], v[124:127], v[34:49]
	v_mfma_f32_32x32x16_f16 v[2:17], v[132:135], v[128:131], v[2:17]
	ds_read_b128 v[120:123], v110 offset:16384
	ds_read_b128 v[124:127], v111
	ds_read_b128 v[128:131], v111 offset:4096
	ds_read_b128 v[132:135], v110 offset:20480
	s_waitcnt lgkmcnt(2)
	v_mfma_f32_32x32x16_f16 v[50:65], v[120:123], v[124:127], v[50:65]
	s_waitcnt lgkmcnt(1)
	v_mfma_f32_32x32x16_f16 v[18:33], v[120:123], v[128:131], v[18:33]
	s_waitcnt lgkmcnt(0)
	v_mfma_f32_32x32x16_f16 v[34:49], v[132:135], v[124:127], v[34:49]
	v_mfma_f32_32x32x16_f16 v[2:17], v[132:135], v[128:131], v[2:17]
	ds_read_b128 v[120:123], v67 offset:16384
	ds_read_b128 v[124:127], v109
	ds_read_b128 v[128:131], v109 offset:4096
	ds_read_b128 v[132:135], v67 offset:20480
	buffer_load_dwordx4 v72, s[4:7], s43 offen lds
	s_mov_b32 m0, s2
	s_nop 0
	buffer_load_dwordx4 v74, s[4:7], s43 offen lds
	s_mov_b32 m0, s3
	s_waitcnt lgkmcnt(2)
	v_mfma_f32_32x32x16_f16 v[50:65], v[120:123], v[124:127], v[50:65]
	buffer_load_dwordx4 v73, s[12:15], s43 offen lds
	s_mov_b32 m0, s18
	s_nop 0
	buffer_load_dwordx4 v75, s[12:15], s43 offen lds
	s_waitcnt vmcnt(8)
	s_barrier
	s_add_i32 s43, s0, 0x880
	s_waitcnt lgkmcnt(1)
	v_mfma_f32_32x32x16_f16 v[18:33], v[120:123], v[128:131], v[18:33]
	s_mov_b32 m0, s19
	s_waitcnt lgkmcnt(0)
	v_mfma_f32_32x32x16_f16 v[34:49], v[132:135], v[124:127], v[34:49]
	v_mfma_f32_32x32x16_f16 v[2:17], v[132:135], v[128:131], v[2:17]
	ds_read_b128 v[120:123], v110 offset:49152
	ds_read_b128 v[124:127], v111 offset:32768
	ds_read_b128 v[128:131], v111 offset:36864
	ds_read_b128 v[132:135], v110 offset:53248
	s_waitcnt lgkmcnt(2)
	v_mfma_f32_32x32x16_f16 v[50:65], v[120:123], v[124:127], v[50:65]
	s_waitcnt lgkmcnt(1)
	v_mfma_f32_32x32x16_f16 v[18:33], v[120:123], v[128:131], v[18:33]
	s_waitcnt lgkmcnt(0)
	v_mfma_f32_32x32x16_f16 v[34:49], v[132:135], v[124:127], v[34:49]
	v_mfma_f32_32x32x16_f16 v[2:17], v[132:135], v[128:131], v[2:17]
	ds_read_b128 v[120:123], v67 offset:49152
	ds_read_b128 v[124:127], v109 offset:32768
	ds_read_b128 v[128:131], v109 offset:36864
	ds_read_b128 v[132:135], v67 offset:53248
	buffer_load_dwordx4 v72, s[4:7], s43 offen lds
	s_mov_b32 m0, s31
	s_nop 0
	buffer_load_dwordx4 v74, s[4:7], s43 offen lds
	s_mov_b32 m0, s33
	s_waitcnt lgkmcnt(2)
	v_mfma_f32_32x32x16_f16 v[50:65], v[120:123], v[124:127], v[50:65]
	buffer_load_dwordx4 v73, s[12:15], s43 offen lds
	s_mov_b32 m0, s34
	s_nop 0
	buffer_load_dwordx4 v75, s[12:15], s43 offen lds
	s_waitcnt vmcnt(8)
	s_barrier
	s_add_i32 s43, s0, 0x900
	s_waitcnt lgkmcnt(1)
	v_mfma_f32_32x32x16_f16 v[18:33], v[120:123], v[128:131], v[18:33]
	s_mov_b32 m0, s35
	s_waitcnt lgkmcnt(0)
	v_mfma_f32_32x32x16_f16 v[34:49], v[132:135], v[124:127], v[34:49]
	v_mfma_f32_32x32x16_f16 v[2:17], v[132:135], v[128:131], v[2:17]
	ds_read_b128 v[120:123], v96
	ds_read_b128 v[124:127], v113
	ds_read_b128 v[128:131], v113 offset:4096
	ds_read_b128 v[132:135], v112 offset:4096
	s_waitcnt lgkmcnt(2)
	v_mfma_f32_32x32x16_f16 v[50:65], v[120:123], v[124:127], v[50:65]
	s_waitcnt lgkmcnt(1)
	v_mfma_f32_32x32x16_f16 v[18:33], v[120:123], v[128:131], v[18:33]
	s_waitcnt lgkmcnt(0)
	v_mfma_f32_32x32x16_f16 v[34:49], v[132:135], v[124:127], v[34:49]
	v_mfma_f32_32x32x16_f16 v[2:17], v[132:135], v[128:131], v[2:17]
	ds_read_b128 v[120:123], v97
	ds_read_b128 v[124:127], v115
	ds_read_b128 v[128:131], v115 offset:4096
	ds_read_b128 v[132:135], v114 offset:4096
	buffer_load_dwordx4 v72, s[4:7], s43 offen lds
	s_mov_b32 m0, s36
	s_nop 0
	buffer_load_dwordx4 v74, s[4:7], s43 offen lds
	s_mov_b32 m0, s37
	s_waitcnt lgkmcnt(2)
	v_mfma_f32_32x32x16_f16 v[50:65], v[120:123], v[124:127], v[50:65]
	buffer_load_dwordx4 v73, s[12:15], s43 offen lds
	s_mov_b32 m0, s38
	s_nop 0
	buffer_load_dwordx4 v75, s[12:15], s43 offen lds
	s_waitcnt vmcnt(8)
	s_barrier
	s_add_i32 s43, s0, 0x980
	s_waitcnt lgkmcnt(1)
	v_mfma_f32_32x32x16_f16 v[18:33], v[120:123], v[128:131], v[18:33]
	s_mov_b32 m0, s39
	s_waitcnt lgkmcnt(0)
	v_mfma_f32_32x32x16_f16 v[34:49], v[132:135], v[124:127], v[34:49]
	v_mfma_f32_32x32x16_f16 v[2:17], v[132:135], v[128:131], v[2:17]
	ds_read_b128 v[120:123], v98
	ds_read_b128 v[124:127], v117
	ds_read_b128 v[128:131], v117 offset:4096
	ds_read_b128 v[132:135], v116 offset:4096
	s_waitcnt lgkmcnt(2)
	v_mfma_f32_32x32x16_f16 v[50:65], v[120:123], v[124:127], v[50:65]
	s_waitcnt lgkmcnt(1)
	v_mfma_f32_32x32x16_f16 v[18:33], v[120:123], v[128:131], v[18:33]
	s_waitcnt lgkmcnt(0)
	v_mfma_f32_32x32x16_f16 v[34:49], v[132:135], v[124:127], v[34:49]
	v_mfma_f32_32x32x16_f16 v[2:17], v[132:135], v[128:131], v[2:17]
	ds_read_b128 v[120:123], v99
	ds_read_b128 v[124:127], v119
	ds_read_b128 v[128:131], v119 offset:4096
	ds_read_b128 v[132:135], v118 offset:4096
	buffer_load_dwordx4 v72, s[4:7], s43 offen lds
	s_mov_b32 m0, s40
	s_nop 0
	buffer_load_dwordx4 v74, s[4:7], s43 offen lds
	s_mov_b32 m0, s41
	s_waitcnt lgkmcnt(2)
	v_mfma_f32_32x32x16_f16 v[50:65], v[120:123], v[124:127], v[50:65]
	buffer_load_dwordx4 v73, s[12:15], s43 offen lds
	s_mov_b32 m0, s42
	s_nop 0
	buffer_load_dwordx4 v75, s[12:15], s43 offen lds
	s_waitcnt vmcnt(8)
	s_barrier
	s_add_i32 s43, s0, 0xa00
	s_waitcnt lgkmcnt(1)
	v_mfma_f32_32x32x16_f16 v[18:33], v[120:123], v[128:131], v[18:33]
	s_mov_b32 m0, s1
	s_waitcnt lgkmcnt(0)
	v_mfma_f32_32x32x16_f16 v[34:49], v[132:135], v[124:127], v[34:49]
	v_mfma_f32_32x32x16_f16 v[2:17], v[132:135], v[128:131], v[2:17]
	ds_read_b128 v[120:123], v110 offset:16384
	ds_read_b128 v[124:127], v111
	ds_read_b128 v[128:131], v111 offset:4096
	ds_read_b128 v[132:135], v110 offset:20480
	s_waitcnt lgkmcnt(2)
	v_mfma_f32_32x32x16_f16 v[50:65], v[120:123], v[124:127], v[50:65]
	s_waitcnt lgkmcnt(1)
	v_mfma_f32_32x32x16_f16 v[18:33], v[120:123], v[128:131], v[18:33]
	s_waitcnt lgkmcnt(0)
	v_mfma_f32_32x32x16_f16 v[34:49], v[132:135], v[124:127], v[34:49]
	v_mfma_f32_32x32x16_f16 v[2:17], v[132:135], v[128:131], v[2:17]
	ds_read_b128 v[120:123], v67 offset:16384
	ds_read_b128 v[124:127], v109
	ds_read_b128 v[128:131], v109 offset:4096
	ds_read_b128 v[132:135], v67 offset:20480
	buffer_load_dwordx4 v72, s[4:7], s43 offen lds
	s_mov_b32 m0, s2
	s_nop 0
	buffer_load_dwordx4 v74, s[4:7], s43 offen lds
	s_mov_b32 m0, s3
	s_waitcnt lgkmcnt(2)
	v_mfma_f32_32x32x16_f16 v[50:65], v[120:123], v[124:127], v[50:65]
	buffer_load_dwordx4 v73, s[12:15], s43 offen lds
	s_mov_b32 m0, s18
	s_nop 0
	buffer_load_dwordx4 v75, s[12:15], s43 offen lds
	s_waitcnt vmcnt(8)
	s_barrier
	s_add_i32 s43, s0, 0xa80
	s_waitcnt lgkmcnt(1)
	v_mfma_f32_32x32x16_f16 v[18:33], v[120:123], v[128:131], v[18:33]
	s_mov_b32 m0, s19
	s_waitcnt lgkmcnt(0)
	v_mfma_f32_32x32x16_f16 v[34:49], v[132:135], v[124:127], v[34:49]
	v_mfma_f32_32x32x16_f16 v[2:17], v[132:135], v[128:131], v[2:17]
	ds_read_b128 v[120:123], v110 offset:49152
	ds_read_b128 v[124:127], v111 offset:32768
	ds_read_b128 v[128:131], v111 offset:36864
	ds_read_b128 v[132:135], v110 offset:53248
	s_waitcnt lgkmcnt(2)
	v_mfma_f32_32x32x16_f16 v[50:65], v[120:123], v[124:127], v[50:65]
	s_waitcnt lgkmcnt(1)
	v_mfma_f32_32x32x16_f16 v[18:33], v[120:123], v[128:131], v[18:33]
	s_waitcnt lgkmcnt(0)
	v_mfma_f32_32x32x16_f16 v[34:49], v[132:135], v[124:127], v[34:49]
	v_mfma_f32_32x32x16_f16 v[2:17], v[132:135], v[128:131], v[2:17]
	ds_read_b128 v[120:123], v67 offset:49152
	ds_read_b128 v[124:127], v109 offset:32768
	ds_read_b128 v[128:131], v109 offset:36864
	ds_read_b128 v[132:135], v67 offset:53248
	buffer_load_dwordx4 v72, s[4:7], s43 offen lds
	s_mov_b32 m0, s31
	s_nop 0
	buffer_load_dwordx4 v74, s[4:7], s43 offen lds
	s_mov_b32 m0, s33
	s_waitcnt lgkmcnt(2)
	v_mfma_f32_32x32x16_f16 v[50:65], v[120:123], v[124:127], v[50:65]
	buffer_load_dwordx4 v73, s[12:15], s43 offen lds
	s_mov_b32 m0, s34
	s_nop 0
	buffer_load_dwordx4 v75, s[12:15], s43 offen lds
	s_waitcnt vmcnt(8)
	s_barrier
	s_add_i32 s43, s0, 0xb00
	s_waitcnt lgkmcnt(1)
	v_mfma_f32_32x32x16_f16 v[18:33], v[120:123], v[128:131], v[18:33]
	s_mov_b32 m0, s35
	s_waitcnt lgkmcnt(0)
	v_mfma_f32_32x32x16_f16 v[34:49], v[132:135], v[124:127], v[34:49]
	v_mfma_f32_32x32x16_f16 v[2:17], v[132:135], v[128:131], v[2:17]
	ds_read_b128 v[120:123], v96
	ds_read_b128 v[124:127], v113
	ds_read_b128 v[128:131], v113 offset:4096
	ds_read_b128 v[132:135], v112 offset:4096
	s_waitcnt lgkmcnt(2)
	v_mfma_f32_32x32x16_f16 v[50:65], v[120:123], v[124:127], v[50:65]
	s_waitcnt lgkmcnt(1)
	v_mfma_f32_32x32x16_f16 v[18:33], v[120:123], v[128:131], v[18:33]
	s_waitcnt lgkmcnt(0)
	v_mfma_f32_32x32x16_f16 v[34:49], v[132:135], v[124:127], v[34:49]
	v_mfma_f32_32x32x16_f16 v[2:17], v[132:135], v[128:131], v[2:17]
	ds_read_b128 v[120:123], v97
	ds_read_b128 v[124:127], v115
	ds_read_b128 v[128:131], v115 offset:4096
	ds_read_b128 v[132:135], v114 offset:4096
	buffer_load_dwordx4 v72, s[4:7], s43 offen lds
	s_mov_b32 m0, s36
	s_nop 0
	buffer_load_dwordx4 v74, s[4:7], s43 offen lds
	s_mov_b32 m0, s37
	s_waitcnt lgkmcnt(2)
	v_mfma_f32_32x32x16_f16 v[50:65], v[120:123], v[124:127], v[50:65]
	buffer_load_dwordx4 v73, s[12:15], s43 offen lds
	s_mov_b32 m0, s38
	s_nop 0
	buffer_load_dwordx4 v75, s[12:15], s43 offen lds
	s_waitcnt vmcnt(8)
	s_barrier
	s_add_i32 s43, s0, 0xb80
	s_waitcnt lgkmcnt(1)
	v_mfma_f32_32x32x16_f16 v[18:33], v[120:123], v[128:131], v[18:33]
	s_mov_b32 m0, s39
	s_waitcnt lgkmcnt(0)
	v_mfma_f32_32x32x16_f16 v[34:49], v[132:135], v[124:127], v[34:49]
	v_mfma_f32_32x32x16_f16 v[2:17], v[132:135], v[128:131], v[2:17]
	ds_read_b128 v[120:123], v98
	ds_read_b128 v[124:127], v117
	ds_read_b128 v[128:131], v117 offset:4096
	ds_read_b128 v[132:135], v116 offset:4096
	s_waitcnt lgkmcnt(2)
	v_mfma_f32_32x32x16_f16 v[50:65], v[120:123], v[124:127], v[50:65]
	s_waitcnt lgkmcnt(1)
	v_mfma_f32_32x32x16_f16 v[18:33], v[120:123], v[128:131], v[18:33]
	s_waitcnt lgkmcnt(0)
	v_mfma_f32_32x32x16_f16 v[34:49], v[132:135], v[124:127], v[34:49]
	v_mfma_f32_32x32x16_f16 v[2:17], v[132:135], v[128:131], v[2:17]
	ds_read_b128 v[120:123], v99
	ds_read_b128 v[124:127], v119
	ds_read_b128 v[128:131], v119 offset:4096
	ds_read_b128 v[132:135], v118 offset:4096
	buffer_load_dwordx4 v72, s[4:7], s43 offen lds
	s_mov_b32 m0, s40
	s_nop 0
	buffer_load_dwordx4 v74, s[4:7], s43 offen lds
	s_mov_b32 m0, s41
	s_waitcnt lgkmcnt(2)
	v_mfma_f32_32x32x16_f16 v[50:65], v[120:123], v[124:127], v[50:65]
	buffer_load_dwordx4 v73, s[12:15], s43 offen lds
	s_mov_b32 m0, s42
	s_nop 0
	buffer_load_dwordx4 v75, s[12:15], s43 offen lds
	s_waitcnt vmcnt(8)
	s_barrier
	s_add_i32 s43, s0, 0xc00
	s_waitcnt lgkmcnt(1)
	v_mfma_f32_32x32x16_f16 v[18:33], v[120:123], v[128:131], v[18:33]
	s_mov_b32 m0, s1
	s_waitcnt lgkmcnt(0)
	v_mfma_f32_32x32x16_f16 v[34:49], v[132:135], v[124:127], v[34:49]
	v_mfma_f32_32x32x16_f16 v[2:17], v[132:135], v[128:131], v[2:17]
	ds_read_b128 v[120:123], v110 offset:16384
	ds_read_b128 v[124:127], v111
	ds_read_b128 v[128:131], v111 offset:4096
	ds_read_b128 v[132:135], v110 offset:20480
	s_waitcnt lgkmcnt(2)
	v_mfma_f32_32x32x16_f16 v[50:65], v[120:123], v[124:127], v[50:65]
	s_waitcnt lgkmcnt(1)
	v_mfma_f32_32x32x16_f16 v[18:33], v[120:123], v[128:131], v[18:33]
	s_waitcnt lgkmcnt(0)
	v_mfma_f32_32x32x16_f16 v[34:49], v[132:135], v[124:127], v[34:49]
	v_mfma_f32_32x32x16_f16 v[2:17], v[132:135], v[128:131], v[2:17]
	ds_read_b128 v[120:123], v67 offset:16384
	ds_read_b128 v[124:127], v109
	ds_read_b128 v[128:131], v109 offset:4096
	ds_read_b128 v[132:135], v67 offset:20480
	buffer_load_dwordx4 v72, s[4:7], s43 offen lds
	s_mov_b32 m0, s2
	s_nop 0
	buffer_load_dwordx4 v74, s[4:7], s43 offen lds
	s_mov_b32 m0, s3
	s_waitcnt lgkmcnt(2)
	v_mfma_f32_32x32x16_f16 v[50:65], v[120:123], v[124:127], v[50:65]
	buffer_load_dwordx4 v73, s[12:15], s43 offen lds
	s_mov_b32 m0, s18
	s_nop 0
	buffer_load_dwordx4 v75, s[12:15], s43 offen lds
	s_waitcnt vmcnt(8)
	s_barrier
	s_add_i32 s43, s0, 0xc80
	s_waitcnt lgkmcnt(1)
	v_mfma_f32_32x32x16_f16 v[18:33], v[120:123], v[128:131], v[18:33]
	s_mov_b32 m0, s19
	s_add_i32 s19, s0, 0xd00
	s_waitcnt lgkmcnt(0)
	v_mfma_f32_32x32x16_f16 v[34:49], v[132:135], v[124:127], v[34:49]
	v_mfma_f32_32x32x16_f16 v[2:17], v[132:135], v[128:131], v[2:17]
	ds_read_b128 v[120:123], v110 offset:49152
	ds_read_b128 v[124:127], v111 offset:32768
	ds_read_b128 v[128:131], v111 offset:36864
	ds_read_b128 v[132:135], v110 offset:53248
	s_waitcnt lgkmcnt(2)
	v_mfma_f32_32x32x16_f16 v[50:65], v[120:123], v[124:127], v[50:65]
	s_waitcnt lgkmcnt(1)
	v_mfma_f32_32x32x16_f16 v[18:33], v[120:123], v[128:131], v[18:33]
	s_waitcnt lgkmcnt(0)
	v_mfma_f32_32x32x16_f16 v[34:49], v[132:135], v[124:127], v[34:49]
	v_mfma_f32_32x32x16_f16 v[2:17], v[132:135], v[128:131], v[2:17]
	ds_read_b128 v[120:123], v67 offset:49152
	ds_read_b128 v[124:127], v109 offset:32768
	ds_read_b128 v[128:131], v109 offset:36864
	ds_read_b128 v[132:135], v67 offset:53248
	buffer_load_dwordx4 v72, s[4:7], s43 offen lds
	s_mov_b32 m0, s31
	s_add_i32 s31, s0, 0xe00
	buffer_load_dwordx4 v74, s[4:7], s43 offen lds
	s_mov_b32 m0, s33
	s_waitcnt lgkmcnt(2)
	v_mfma_f32_32x32x16_f16 v[50:65], v[120:123], v[124:127], v[50:65]
	buffer_load_dwordx4 v73, s[12:15], s43 offen lds
	s_mov_b32 m0, s34
	s_nop 0
	buffer_load_dwordx4 v75, s[12:15], s43 offen lds
	s_waitcnt vmcnt(8)
	s_barrier
	s_mov_b32 m0, s35
	s_waitcnt lgkmcnt(1)
	v_mfma_f32_32x32x16_f16 v[18:33], v[120:123], v[128:131], v[18:33]
	s_waitcnt lgkmcnt(0)
	v_mfma_f32_32x32x16_f16 v[34:49], v[132:135], v[124:127], v[34:49]
	v_mfma_f32_32x32x16_f16 v[2:17], v[132:135], v[128:131], v[2:17]
	ds_read_b128 v[120:123], v96
	ds_read_b128 v[124:127], v113
	ds_read_b128 v[128:131], v113 offset:4096
	ds_read_b128 v[132:135], v112 offset:4096
	s_waitcnt lgkmcnt(2)
	v_mfma_f32_32x32x16_f16 v[50:65], v[120:123], v[124:127], v[50:65]
	s_waitcnt lgkmcnt(1)
	v_mfma_f32_32x32x16_f16 v[18:33], v[120:123], v[128:131], v[18:33]
	s_waitcnt lgkmcnt(0)
	v_mfma_f32_32x32x16_f16 v[34:49], v[132:135], v[124:127], v[34:49]
	v_mfma_f32_32x32x16_f16 v[2:17], v[132:135], v[128:131], v[2:17]
	ds_read_b128 v[120:123], v97
	ds_read_b128 v[124:127], v115
	ds_read_b128 v[128:131], v115 offset:4096
	ds_read_b128 v[132:135], v114 offset:4096
	buffer_load_dwordx4 v72, s[4:7], s19 offen lds
	s_mov_b32 m0, s36
	s_nop 0
	buffer_load_dwordx4 v74, s[4:7], s19 offen lds
	s_mov_b32 m0, s37
	s_waitcnt lgkmcnt(2)
	v_mfma_f32_32x32x16_f16 v[50:65], v[120:123], v[124:127], v[50:65]
	buffer_load_dwordx4 v73, s[12:15], s19 offen lds
	s_mov_b32 m0, s38
	s_nop 0
	buffer_load_dwordx4 v75, s[12:15], s19 offen lds
	s_waitcnt vmcnt(8)
	s_barrier
	s_add_i32 s19, s0, 0xd80
	s_waitcnt lgkmcnt(1)
	v_mfma_f32_32x32x16_f16 v[18:33], v[120:123], v[128:131], v[18:33]
	s_mov_b32 m0, s39
	s_ashr_i32 s0, s23, 31
	s_xor_b32 s0, s0, s25
	s_waitcnt lgkmcnt(0)
	v_mfma_f32_32x32x16_f16 v[34:49], v[132:135], v[124:127], v[34:49]
	v_mfma_f32_32x32x16_f16 v[2:17], v[132:135], v[128:131], v[2:17]
	ds_read_b128 v[120:123], v98
	ds_read_b128 v[124:127], v117
	ds_read_b128 v[128:131], v117 offset:4096
	ds_read_b128 v[132:135], v116 offset:4096
	s_waitcnt lgkmcnt(2)
	v_mfma_f32_32x32x16_f16 v[50:65], v[120:123], v[124:127], v[50:65]
	s_waitcnt lgkmcnt(1)
	v_mfma_f32_32x32x16_f16 v[18:33], v[120:123], v[128:131], v[18:33]
	s_waitcnt lgkmcnt(0)
	v_mfma_f32_32x32x16_f16 v[34:49], v[132:135], v[124:127], v[34:49]
	v_mfma_f32_32x32x16_f16 v[2:17], v[132:135], v[128:131], v[2:17]
	ds_read_b128 v[120:123], v99
	ds_read_b128 v[124:127], v119
	ds_read_b128 v[128:131], v119 offset:4096
	ds_read_b128 v[132:135], v118 offset:4096
	buffer_load_dwordx4 v72, s[4:7], s19 offen lds
	s_mov_b32 m0, s40
	s_nop 0
	buffer_load_dwordx4 v74, s[4:7], s19 offen lds
	s_mov_b32 m0, s41
	s_waitcnt lgkmcnt(2)
	v_mfma_f32_32x32x16_f16 v[50:65], v[120:123], v[124:127], v[50:65]
	buffer_load_dwordx4 v73, s[12:15], s19 offen lds
	s_mov_b32 m0, s42
	s_nop 0
	buffer_load_dwordx4 v75, s[12:15], s19 offen lds
	s_waitcnt vmcnt(8)
	s_barrier
	s_mov_b32 m0, s1
	s_waitcnt lgkmcnt(1)
	v_mfma_f32_32x32x16_f16 v[18:33], v[120:123], v[128:131], v[18:33]
	s_abs_i32 s1, s23
	s_waitcnt lgkmcnt(0)
	v_mfma_f32_32x32x16_f16 v[34:49], v[132:135], v[124:127], v[34:49]
	v_mfma_f32_32x32x16_f16 v[2:17], v[132:135], v[128:131], v[2:17]
	ds_read_b128 v[120:123], v110 offset:16384
	ds_read_b128 v[124:127], v111
	ds_read_b128 v[128:131], v111 offset:4096
	ds_read_b128 v[132:135], v110 offset:20480
	s_waitcnt lgkmcnt(2)
	v_mfma_f32_32x32x16_f16 v[50:65], v[120:123], v[124:127], v[50:65]
	s_waitcnt lgkmcnt(1)
	v_mfma_f32_32x32x16_f16 v[18:33], v[120:123], v[128:131], v[18:33]
	s_waitcnt lgkmcnt(0)
	v_mfma_f32_32x32x16_f16 v[34:49], v[132:135], v[124:127], v[34:49]
	v_mfma_f32_32x32x16_f16 v[2:17], v[132:135], v[128:131], v[2:17]
	ds_read_b128 v[120:123], v67 offset:16384
	ds_read_b128 v[124:127], v109
	ds_read_b128 v[128:131], v109 offset:4096
	ds_read_b128 v[132:135], v67 offset:20480
	buffer_load_dwordx4 v72, s[4:7], s31 offen lds
	s_mov_b32 m0, s2
	s_mul_hi_u32 s2, s1, s26
	buffer_load_dwordx4 v74, s[4:7], s31 offen lds
	s_mov_b32 m0, s3
	s_mul_i32 s3, s2, s24
	s_waitcnt lgkmcnt(2)
	v_mfma_f32_32x32x16_f16 v[50:65], v[120:123], v[124:127], v[50:65]
	buffer_load_dwordx4 v73, s[12:15], s31 offen lds
	s_mov_b32 m0, s18
	s_sub_i32 s1, s1, s3
	buffer_load_dwordx4 v75, s[12:15], s31 offen lds
	s_waitcnt vmcnt(8)
	s_barrier
	s_add_i32 s3, s2, 1
	s_waitcnt lgkmcnt(1)
	v_mfma_f32_32x32x16_f16 v[18:33], v[120:123], v[128:131], v[18:33]
	s_sub_i32 s14, s1, s24
	s_cmp_ge_u32 s1, s24
	s_cselect_b32 s2, s3, s2
	s_cselect_b32 s1, s14, s1
	s_add_i32 s3, s2, 1
	s_cmp_ge_u32 s1, s24
	s_cselect_b32 s1, s3, s2
	s_waitcnt lgkmcnt(0)
	v_mfma_f32_32x32x16_f16 v[34:49], v[132:135], v[124:127], v[34:49]
	s_xor_b32 s1, s1, s0
	s_sub_i32 s0, s1, s0
	s_mul_i32 s1, s0, s21
	s_sub_i32 s15, s23, s1
	s_lshl_b32 s2, s15, 7
	s_lshl_b32 s14, s0, 7
	s_ashr_i32 s3, s2, 31
	v_mfma_f32_32x32x16_f16 v[2:17], v[132:135], v[128:131], v[2:17]
	ds_read_b128 v[120:123], v110 offset:49152
	ds_read_b128 v[124:127], v111 offset:32768
	ds_read_b128 v[128:131], v111 offset:36864
	ds_read_b128 v[132:135], v110 offset:53248
	s_waitcnt lgkmcnt(2)
	v_mfma_f32_32x32x16_f16 v[50:65], v[120:123], v[124:127], v[50:65]
	s_waitcnt lgkmcnt(1)
	v_mfma_f32_32x32x16_f16 v[18:33], v[120:123], v[128:131], v[18:33]
	s_waitcnt lgkmcnt(0)
	v_mfma_f32_32x32x16_f16 v[34:49], v[132:135], v[124:127], v[34:49]
	v_mfma_f32_32x32x16_f16 v[2:17], v[132:135], v[128:131], v[2:17]
	ds_read_b128 v[120:123], v67 offset:49152
	ds_read_b128 v[124:127], v109 offset:32768
	ds_read_b128 v[128:131], v109 offset:36864
	ds_read_b128 v[132:135], v67 offset:53248
	s_waitcnt vmcnt(4)
	s_barrier
	s_waitcnt lgkmcnt(2)
	v_mfma_f32_32x32x16_f16 v[50:65], v[120:123], v[124:127], v[50:65]
	s_waitcnt lgkmcnt(1)
	v_mfma_f32_32x32x16_f16 v[18:33], v[120:123], v[128:131], v[18:33]
	s_waitcnt lgkmcnt(0)
	v_mfma_f32_32x32x16_f16 v[34:49], v[132:135], v[124:127], v[34:49]
	v_mfma_f32_32x32x16_f16 v[2:17], v[132:135], v[128:131], v[2:17]
	ds_read_b128 v[120:123], v96
	ds_read_b128 v[124:127], v113
	ds_read_b128 v[128:131], v113 offset:4096
	ds_read_b128 v[110:113], v112 offset:4096
	s_waitcnt lgkmcnt(2)
	v_mfma_f32_32x32x16_f16 v[50:65], v[120:123], v[124:127], v[50:65]
	s_waitcnt lgkmcnt(1)
	v_mfma_f32_32x32x16_f16 v[18:33], v[120:123], v[128:131], v[18:33]
	s_waitcnt lgkmcnt(0)
	v_mfma_f32_32x32x16_f16 v[34:49], v[110:113], v[124:127], v[34:49]
	ds_read_b128 v[120:123], v97
	ds_read_b128 v[124:127], v115
	ds_read_b128 v[132:135], v115 offset:4096
	s_waitcnt lgkmcnt(1)
	v_mfma_f32_32x32x16_f16 v[50:65], v[120:123], v[124:127], v[50:65]
	s_waitcnt lgkmcnt(0)
	v_mfma_f32_32x32x16_f16 v[18:33], v[120:123], v[132:135], v[18:33]
	ds_read_b128 v[120:123], v114 offset:4096
	s_waitcnt vmcnt(0)
	s_barrier
	v_mfma_f32_32x32x16_f16 v[2:17], v[110:113], v[128:131], v[2:17]
	s_waitcnt lgkmcnt(0)
	v_mfma_f32_32x32x16_f16 v[34:49], v[120:123], v[124:127], v[34:49]
	ds_read_b128 v[124:127], v98
	ds_read_b128 v[136:139], v117
	ds_read_b128 v[140:143], v117 offset:4096
	ds_read_b128 v[114:117], v116 offset:4096
	s_waitcnt lgkmcnt(2)
	v_mfma_f32_32x32x16_f16 v[50:65], v[124:127], v[136:139], v[50:65]
	s_waitcnt lgkmcnt(1)
	v_mfma_f32_32x32x16_f16 v[18:33], v[124:127], v[140:143], v[18:33]
	v_mfma_f32_32x32x16_f16 v[2:17], v[120:123], v[132:135], v[2:17]
	s_waitcnt lgkmcnt(0)
	v_mfma_f32_32x32x16_f16 v[34:49], v[114:117], v[136:139], v[34:49]
	ds_read_b128 v[124:127], v99
	ds_read_b128 v[136:139], v119
	ds_read_b128 v[144:147], v119 offset:4096
	s_waitcnt lgkmcnt(1)
	v_mfma_f32_32x32x16_f16 v[50:65], v[124:127], v[136:139], v[50:65]
	s_waitcnt lgkmcnt(0)
	v_mfma_f32_32x32x16_f16 v[18:33], v[124:127], v[144:147], v[18:33]
	ds_read_b128 v[124:127], v118 offset:4096
	s_waitcnt lgkmcnt(0)
	s_barrier
	s_nop 8
	ds_write_b128 v100, v[50:53]
	ds_write_b128 v101, v[54:57]
	v_mfma_f32_32x32x16_f16 v[2:17], v[114:117], v[140:143], v[2:17]
	s_waitcnt lgkmcnt(2)
	v_mfma_f32_32x32x16_f16 v[2:17], v[124:127], v[144:147], v[2:17]
	v_mfma_f32_32x32x16_f16 v[34:49], v[124:127], v[136:139], v[34:49]
	ds_write_b128 v102, v[58:61]
	ds_write_b128 v103, v[62:65]
	s_nop 9
	ds_write_b128 v104, v[34:37]
	ds_write_b128 v105, v[38:41]
	ds_write_b128 v106, v[42:45]
	ds_write_b128 v107, v[46:49]
	ds_write_b128 v100, v[18:21] offset:16384
	ds_write_b128 v101, v[22:25] offset:16384
	ds_write_b128 v102, v[26:29] offset:16384
	ds_write_b128 v103, v[30:33] offset:16384
	ds_write_b128 v104, v[2:5] offset:16384
	ds_write_b128 v105, v[6:9] offset:16384
	ds_write_b128 v106, v[10:13] offset:16384
	ds_write_b128 v107, v[14:17] offset:16384
	v_or_b32_e32 v25, s14, v1
	s_waitcnt lgkmcnt(0)
	s_barrier
	v_mov_b64_e32 v[10:11], v[160:161]
	v_mov_b64_e32 v[12:13], v[162:163]
	v_mov_b64_e32 v[6:7], v[176:177]
	v_mov_b64_e32 v[8:9], v[178:179]
	v_mov_b64_e32 v[2:3], v[180:181]
	v_mov_b64_e32 v[4:5], v[182:183]
	v_add_u32_e32 v14, 0, v85
	v_add_u32_e32 v18, s28, v85
	ds_read_b128 v[14:17], v14
	ds_read_b128 v[26:29], v18
	v_mov_b64_e32 v[18:19], v[164:165]
	v_mov_b64_e32 v[20:21], v[166:167]
	s_waitcnt lgkmcnt(0)
	v_pk_add_f32 v[16:17], v[16:17], v[28:29]
	v_add_f32_e32 v35, v14, v26
	v_mov_b32_e32 v34, v27
	v_cvt_f32_f16_e32 v30, v11
	v_cvt_f32_f16_sdwa v31, v11 dst_sel:DWORD dst_unused:UNUSED_PAD src0_sel:WORD_1
	v_add_u32_e32 v11, 0, v86
	v_pk_add_f32 v[16:17], v[8:9], v[16:17]
	ds_read_b128 v[26:29], v11
	v_add_u32_e32 v11, s28, v86
	v_pk_add_f32 v[36:37], v[16:17], v[30:31]
	ds_read_b128 v[30:33], v11
	v_cvt_f32_f16_e32 v38, v13
	v_cvt_f32_f16_sdwa v39, v13 dst_sel:DWORD dst_unused:UNUSED_PAD src0_sel:WORD_1
	v_mov_b32_e32 v16, v2
	v_mov_b32_e32 v17, v3
	s_waitcnt lgkmcnt(0)
	v_pk_add_f32 v[28:29], v[28:29], v[32:33]
	v_cvt_f32_f16_e32 v32, v10
	v_pk_add_f32 v[28:29], v[4:5], v[28:29]
	v_pk_mov_b32 v[16:17], v[26:27], v[16:17] op_sel:[1,0]
	v_pk_add_f32 v[28:29], v[28:29], v[38:39]
	v_cvt_f32_f16_e32 v38, v12
	v_add_f32_e32 v26, v26, v30
	v_cvt_f32_f16_sdwa v33, v10 dst_sel:DWORD dst_unused:UNUSED_PAD src0_sel:WORD_1
	v_cvt_f32_f16_sdwa v30, v12 dst_sel:DWORD dst_unused:UNUSED_PAD src0_sel:WORD_1
	v_pk_mov_b32 v[14:15], v[14:15], v[6:7] op_sel:[1,0]
	v_mov_b32_e32 v10, v31
	v_mov_b32_e32 v11, v26
	v_pk_add_f32 v[44:45], v[14:15], v[34:35]
	v_mov_b32_e32 v12, v7
	v_mov_b32_e32 v13, v32
	v_pk_add_f32 v[10:11], v[16:17], v[10:11]
	v_pk_add_f32 v[46:47], v[12:13], v[44:45]
	v_mov_b32_e32 v22, v3
	v_mov_b32_e32 v23, v38
	v_pk_add_f32 v[48:49], v[22:23], v[10:11]
	v_mov_b32_e32 v10, v33
	v_mov_b32_e32 v11, v47
	v_pk_add_f32 v[50:51], v[46:47], v[10:11]
	v_mov_b64_e32 v[14:15], v[168:169]
	v_mov_b64_e32 v[16:17], v[170:171]
	v_mov_b64_e32 v[10:11], v[172:173]
	v_mov_b64_e32 v[12:13], v[174:175]
	v_mov_b32_e32 v31, v49
	v_pk_add_f32 v[40:41], v[48:49], v[30:31]
	v_pk_mov_b32 v[30:31], v[34:35], v[44:45] op_sel:[1,0]
	v_mov_b32_e32 v27, v44
	v_mov_b32_e32 v3, v7
	v_pk_add_f32 v[30:31], v[6:7], v[30:31]
	v_mov_b32_e32 v39, v33
	v_pk_add_f32 v[26:27], v[2:3], v[26:27]
	v_pk_add_f32 v[30:31], v[30:31], v[32:33]
	v_pk_add_f32 v[26:27], v[26:27], v[38:39]
	v_pk_mul_f32 v[32:33], v[46:47], v[46:47]
	v_pk_add_f32 v[34:35], v[30:31], v[26:27]
	v_pk_mul_f32 v[26:27], v[30:31], v[26:27]
	v_mov_b32_e32 v51, v33
	v_pk_mul_f32 v[32:33], v[48:49], v[48:49]
	v_mov_b32_e32 v35, v27
	v_pk_mul_f32 v[26:27], v[40:41], v[40:41]
	v_mov_b32_e32 v32, v40
	v_mov_b32_e32 v67, v26
	v_pk_add_f32 v[32:33], v[50:51], v[32:33]
	v_pk_add_f32 v[26:27], v[34:35], v[66:67]
	v_pk_mul_f32 v[30:31], v[36:37], v[36:37]
	v_pk_mul_f32 v[34:35], v[28:29], v[28:29]
	v_pk_add_f32 v[26:27], v[32:33], v[26:27]
	v_mov_b32_e32 v32, v36
	v_mov_b32_e32 v33, v30
	v_mov_b32_e32 v38, v28
	v_mov_b32_e32 v39, v34
	v_pk_add_f32 v[32:33], v[32:33], v[38:39]
	v_mov_b32_e32 v30, v37
	v_mov_b32_e32 v34, v29
	v_pk_add_f32 v[26:27], v[26:27], v[32:33]
	v_pk_add_f32 v[30:31], v[30:31], v[34:35]
	v_pk_add_f32 v[26:27], v[26:27], v[30:31]
	s_nop 1
	v_mov_b32_dpp v32, v26 row_mirror row_mask:0xf bank_mask:0xf
	v_mov_b32_dpp v33, v27 row_mirror row_mask:0xf bank_mask:0xf
	v_cvt_pk_f16_f32 v39, v28, v29
	v_cvt_pk_f16_f32 v37, v36, v37
	s_waitcnt lgkmcnt(0)
	v_pk_add_f32 v[26:27], v[26:27], v[32:33]
	s_nop 1
	v_mov_b32_dpp v32, v26 row_half_mirror row_mask:0xf bank_mask:0xf
	v_mov_b32_dpp v33, v27 row_half_mirror row_mask:0xf bank_mask:0xf
	v_cvt_pk_f16_f32 v36, v47, v50
	v_cvt_pk_f16_f32 v38, v49, v40
	s_waitcnt lgkmcnt(0)
	v_pk_add_f32 v[26:27], v[26:27], v[32:33]
	s_nop 1
	v_mov_b32_dpp v28, v26 quad_perm:[2,3,0,1] row_mask:0xf bank_mask:0xf
	v_mov_b32_dpp v29, v27 quad_perm:[2,3,0,1] row_mask:0xf bank_mask:0xf
	v_or_b32_e32 v32, s2, v78
	v_mul_lo_u32 v24, v25, s30
	v_add_lshl_u32 v24, v32, v24, 1
	buffer_store_dwordx4 v[36:39], v24, s[8:11], 0 offen sc1
	s_waitcnt lgkmcnt(0)
	v_pk_add_f32 v[26:27], v[26:27], v[28:29]
	s_lshl_b32 s2, s15, 4
	v_mov_b32_e32 v24, v7
	s_nop 1
	v_mov_b32_dpp v28, v26 quad_perm:[1,0,3,2] row_mask:0xf bank_mask:0xf
	v_mov_b32_dpp v29, v27 quad_perm:[1,0,3,2] row_mask:0xf bank_mask:0xf
	s_and_saveexec_b64 s[0:1], vcc
	s_cbranch_execz .LBB9_5
	s_waitcnt lgkmcnt(0)
	v_pk_add_f32 v[64:65], v[26:27], v[28:29]
	v_lshl_add_u32 v23, v25, 6, s2
	v_mov_b32_e32 v67, v66
	s_mov_b32 s18, s10
	s_mov_b32 s19, s11
	buffer_store_dwordx4 v[64:67], v23, s[16:19], 0 offen sc1
